# baseline (speedup 1.0000x reference)
.LBB1_3:
	s_waitcnt lgkmcnt(0)
	v_mfma_f32_32x32x16_f16 a[0:15], v[18:21], v[74:77], a[0:15]
	s_add_i32 s31, s30, 1
	s_cmp_lg_u32 s30, 2
	s_cselect_b32 s91, s31, 0
	s_mul_i32 s30, s30, 0x9000
	s_mul_i32 s92, s91, 0x9000
	s_add_i32 s96, s92, 0x9000
	s_cmp_lg_u32 s91, 2
	s_cselect_b32 s96, s96, 0
	s_add_i32 s96, s96, s93
	s_mov_b32 m0, s96
	v_add_u32_e32 v147, s30, v208
	global_load_lds_dwordx4 v164, s[94:95]
	s_add_u32 m0, s96, 0x1000
	v_add_u32_e32 v2, s30, v209
	global_load_lds_dwordx4 v165, s[94:95]
	s_add_u32 m0, s96, 0x2000
	v_add_u32_e32 v3, s30, v210
	global_load_lds_dwordx4 v166, s[94:95]
	s_add_u32 m0, s96, 0x3000
	v_add_u32_e32 v146, s92, v141
	global_load_lds_dwordx4 v167, s[94:95]
	s_add_u32 s30, s35, s20
	s_addc_u32 s31, s84, s21
	s_add_u32 m0, s96, 0x4000
	s_load_dwordx16 s[68:83], s[30:31], 0x80
	global_load_lds_dwordx4 v168, s[94:95]
	s_add_u32 m0, s96, 0x5000
	s_load_dwordx16 s[52:67], s[30:31], 0x8080
	global_load_lds_dwordx4 v169, s[94:95]
	s_add_u32 m0, s96, 0x6000
	ds_read_b128 v[90:93], v145
	global_load_lds_dwordx4 v170, s[94:95]
	s_add_u32 m0, s96, 0x7000
	ds_read_b128 v[82:85], v145 offset:2048
	global_load_lds_dwordx4 v171, s[94:95]
	v_mfma_f32_32x32x16_f16 a[240:255], v[38:41], v[74:77], a[240:255]
	ds_read_b128 v[50:53], v147
	v_pk_mul_f16 v148, v46, v136
	v_pk_mul_f16 v149, v42, v137
	v_pk_mul_f16 v150, v47, v136
	v_pk_mul_f16 v151, v43, v137
	v_mfma_f32_32x32x16_f16 a[16:31], v[18:21], v[126:129], a[16:31]
	ds_read_b128 v[54:57], v147 offset:4096
	v_pk_mul_f16 v152, v48, v136
	v_pk_mul_f16 v153, v44, v137
	v_pk_mul_f16 v154, v49, v136
	v_pk_mul_f16 v155, v45, v137
	v_mfma_f32_32x32x16_f16 a[224:239], v[38:41], v[126:129], a[224:239]
	ds_read_b128 v[58:61], v147 offset:8192
	v_pk_mul_f16 v156, v46, v140
	v_pk_mul_f16 v157, v42, v139
	v_pk_mul_f16 v158, v47, v140
	v_pk_mul_f16 v159, v43, v139
	v_mfma_f32_32x32x16_f16 a[32:47], v[18:21], v[122:125], a[32:47]
	ds_read_b128 v[62:65], v147 offset:12288
	v_pk_mul_f16 v160, v48, v140
	v_pk_mul_f16 v161, v44, v139
	v_pk_mul_f16 v162, v49, v140
	v_pk_mul_f16 v163, v45, v139
	v_mfma_f32_32x32x16_f16 a[208:223], v[38:41], v[122:125], a[208:223]
	ds_read_b128 v[66:69], v147 offset:16384
	v_pk_max_f16 v148, v148, v149
	v_pk_max_f16 v150, v150, v151
	v_pk_max_f16 v152, v152, v153
	v_pk_max_f16 v154, v154, v155
	v_mfma_f32_32x32x16_f16 a[48:63], v[18:21], v[118:121], a[48:63]
	ds_read_b128 v[70:73], v147 offset:20480
	v_pk_max_f16 v156, v156, v157
	v_pk_max_f16 v158, v158, v159
	v_pk_max_f16 v160, v160, v161
	v_pk_max_f16 v162, v162, v163
	v_mfma_f32_32x32x16_f16 a[192:207], v[38:41], v[118:121], a[192:207]
	ds_read_b128 v[78:81], v147 offset:24576
	v_cndmask_b32_e64 v114, v1, v148, s[36:37]
	s_mov_b64 vcc, s[38:39]
	v_cndmask_b32_sdwa v114, v1, v148, vcc dst_sel:WORD_1 dst_unused:UNUSED_PRESERVE src0_sel:WORD_1 src1_sel:WORD_1
	v_cndmask_b32_e64 v115, v1, v150, s[40:41]
	s_mov_b64 vcc, s[42:43]
	v_cndmask_b32_sdwa v115, v1, v150, vcc dst_sel:WORD_1 dst_unused:UNUSED_PRESERVE src0_sel:WORD_1 src1_sel:WORD_1
	v_mfma_f32_32x32x16_f16 a[64:79], v[18:21], v[106:109], a[64:79]
	ds_read_b128 v[102:105], v147 offset:28672
	v_cndmask_b32_e64 v116, v1, v152, s[44:45]
	s_mov_b64 vcc, s[46:47]
	v_cndmask_b32_sdwa v116, v1, v152, vcc dst_sel:WORD_1 dst_unused:UNUSED_PRESERVE src0_sel:WORD_1 src1_sel:WORD_1
	v_cndmask_b32_e64 v117, v1, v154, s[48:49]
	s_mov_b64 vcc, s[50:51]
	v_cndmask_b32_sdwa v117, v1, v154, vcc dst_sel:WORD_1 dst_unused:UNUSED_PRESERVE src0_sel:WORD_1 src1_sel:WORD_1
	v_mfma_f32_32x32x16_f16 a[176:191], v[38:41], v[106:109], a[176:191]
	v_cndmask_b32_e64 v110, v138, v156, s[4:5]
	s_mov_b64 vcc, s[6:7]
	v_cndmask_b32_sdwa v110, v138, v156, vcc dst_sel:WORD_1 dst_unused:UNUSED_PRESERVE src0_sel:WORD_1 src1_sel:WORD_1
	v_cndmask_b32_e64 v111, v138, v158, s[8:9]
	s_mov_b64 vcc, s[10:11]
	v_cndmask_b32_sdwa v111, v138, v158, vcc dst_sel:WORD_1 dst_unused:UNUSED_PRESERVE src0_sel:WORD_1 src1_sel:WORD_1
	v_mfma_f32_32x32x16_f16 a[112:127], v[18:21], v[98:101], a[112:127]
	v_cndmask_b32_e64 v112, v138, v160, s[12:13]
	s_mov_b64 vcc, s[14:15]
	v_cndmask_b32_sdwa v112, v138, v160, vcc dst_sel:WORD_1 dst_unused:UNUSED_PRESERVE src0_sel:WORD_1 src1_sel:WORD_1
	v_cndmask_b32_e64 v113, v138, v162, s[16:17]
	s_mov_b64 vcc, s[18:19]
	v_cndmask_b32_sdwa v113, v138, v162, vcc dst_sel:WORD_1 dst_unused:UNUSED_PRESERVE src0_sel:WORD_1 src1_sel:WORD_1
	v_mfma_f32_32x32x16_f16 a[160:175], v[38:41], v[98:101], a[160:175]
	v_pk_add_f16 v148, v115, v114
	v_pk_add_f16 v149, v116, v117
	v_mfma_f32_32x32x16_f16 a[128:143], v[18:21], v[94:97], a[128:143]
	v_pk_add_f16 v150, v111, v110
	v_pk_add_f16 v151, v112, v113
	v_mfma_f32_32x32x16_f16 a[144:159], v[38:41], v[94:97], a[144:159]
	v_pk_add_f16 v148, v148, v149
	v_pk_add_f16 v150, v150, v151
	v_mfma_f32_32x32x16_f16 a[80:95], v[18:21], v[86:89], a[80:95]
	v_dot2c_f32_f16_e32 v134, 0x3c003c00, v148
	v_dot2c_f32_f16_e32 v135, 0x3c003c00, v150
	v_mfma_f32_32x32x16_f16 a[96:111], v[38:41], v[86:89], a[96:111]
	s_waitcnt lgkmcnt(0)
	v_mfma_f32_32x32x16_f16 a[0:15], v[114:117], v[50:53], a[0:15]
	s_load_dwordx16 s[36:51], s[30:31], 0xc0
	s_load_dwordx16 s[4:19], s[30:31], 0x80c0
	ds_read_b128 v[46:49], v145 offset:32
	ds_read_b128 v[42:45], v145 offset:2080
	v_mfma_f32_32x32x16_f16 a[240:255], v[110:113], v[50:53], a[240:255]
	ds_read_b128 v[74:77], v2
	v_pk_mul_f16 v148, v90, v136
	v_pk_mul_f16 v149, v82, v137
	v_pk_mul_f16 v150, v91, v136
	v_pk_mul_f16 v151, v83, v137
	v_mfma_f32_32x32x16_f16 a[16:31], v[114:117], v[54:57], a[16:31]
	ds_read_b128 v[126:129], v2 offset:4096
	v_pk_mul_f16 v152, v92, v136
	v_pk_mul_f16 v153, v84, v137
	v_pk_mul_f16 v154, v93, v136
	v_pk_mul_f16 v155, v85, v137
	v_mfma_f32_32x32x16_f16 a[224:239], v[110:113], v[54:57], a[224:239]
	ds_read_b128 v[122:125], v2 offset:8192
	v_pk_mul_f16 v156, v90, v140
	v_pk_mul_f16 v157, v82, v139
	v_pk_mul_f16 v158, v91, v140
	v_pk_mul_f16 v159, v83, v139
	v_mfma_f32_32x32x16_f16 a[32:47], v[114:117], v[58:61], a[32:47]
	ds_read_b128 v[118:121], v2 offset:12288
	v_pk_mul_f16 v160, v92, v140
	v_pk_mul_f16 v161, v84, v139
	v_pk_mul_f16 v162, v93, v140
	v_pk_mul_f16 v163, v85, v139
	v_mfma_f32_32x32x16_f16 a[208:223], v[110:113], v[58:61], a[208:223]
	ds_read_b128 v[106:109], v2 offset:16384
	v_pk_max_f16 v148, v148, v149
	v_pk_max_f16 v150, v150, v151
	v_pk_max_f16 v152, v152, v153
	v_pk_max_f16 v154, v154, v155
	v_mfma_f32_32x32x16_f16 a[48:63], v[114:117], v[62:65], a[48:63]
	ds_read_b128 v[98:101], v2 offset:20480
	v_pk_max_f16 v156, v156, v157
	v_pk_max_f16 v158, v158, v159
	v_pk_max_f16 v160, v160, v161
	v_pk_max_f16 v162, v162, v163
	v_mfma_f32_32x32x16_f16 a[192:207], v[110:113], v[62:65], a[192:207]
	ds_read_b128 v[94:97], v2 offset:24576
	v_cndmask_b32_e64 v18, v1, v148, s[68:69]
	s_mov_b64 vcc, s[70:71]
	v_cndmask_b32_sdwa v18, v1, v148, vcc dst_sel:WORD_1 dst_unused:UNUSED_PRESERVE src0_sel:WORD_1 src1_sel:WORD_1
	v_cndmask_b32_e64 v19, v1, v150, s[72:73]
	s_mov_b64 vcc, s[74:75]
	v_cndmask_b32_sdwa v19, v1, v150, vcc dst_sel:WORD_1 dst_unused:UNUSED_PRESERVE src0_sel:WORD_1 src1_sel:WORD_1
	v_mfma_f32_32x32x16_f16 a[64:79], v[114:117], v[66:69], a[64:79]
	ds_read_b128 v[86:89], v2 offset:28672
	v_cndmask_b32_e64 v20, v1, v152, s[76:77]
	s_mov_b64 vcc, s[78:79]
	v_cndmask_b32_sdwa v20, v1, v152, vcc dst_sel:WORD_1 dst_unused:UNUSED_PRESERVE src0_sel:WORD_1 src1_sel:WORD_1
	v_cndmask_b32_e64 v21, v1, v154, s[80:81]
	s_mov_b64 vcc, s[82:83]
	v_cndmask_b32_sdwa v21, v1, v154, vcc dst_sel:WORD_1 dst_unused:UNUSED_PRESERVE src0_sel:WORD_1 src1_sel:WORD_1
	v_mfma_f32_32x32x16_f16 a[176:191], v[110:113], v[66:69], a[176:191]
	v_cndmask_b32_e64 v38, v138, v156, s[52:53]
	s_mov_b64 vcc, s[54:55]
	v_cndmask_b32_sdwa v38, v138, v156, vcc dst_sel:WORD_1 dst_unused:UNUSED_PRESERVE src0_sel:WORD_1 src1_sel:WORD_1
	v_cndmask_b32_e64 v39, v138, v158, s[56:57]
	s_mov_b64 vcc, s[58:59]
	v_cndmask_b32_sdwa v39, v138, v158, vcc dst_sel:WORD_1 dst_unused:UNUSED_PRESERVE src0_sel:WORD_1 src1_sel:WORD_1
	v_mfma_f32_32x32x16_f16 a[112:127], v[114:117], v[70:73], a[112:127]
	v_cndmask_b32_e64 v40, v138, v160, s[60:61]
	s_mov_b64 vcc, s[62:63]
	v_cndmask_b32_sdwa v40, v138, v160, vcc dst_sel:WORD_1 dst_unused:UNUSED_PRESERVE src0_sel:WORD_1 src1_sel:WORD_1
	v_cndmask_b32_e64 v41, v138, v162, s[64:65]
	s_mov_b64 vcc, s[66:67]
	v_cndmask_b32_sdwa v41, v138, v162, vcc dst_sel:WORD_1 dst_unused:UNUSED_PRESERVE src0_sel:WORD_1 src1_sel:WORD_1
	v_mfma_f32_32x32x16_f16 a[160:175], v[110:113], v[70:73], a[160:175]
	v_pk_add_f16 v148, v19, v18
	v_pk_add_f16 v149, v20, v21
	v_mfma_f32_32x32x16_f16 a[128:143], v[114:117], v[78:81], a[128:143]
	v_pk_add_f16 v150, v39, v38
	v_pk_add_f16 v151, v40, v41
	v_mfma_f32_32x32x16_f16 a[144:159], v[110:113], v[78:81], a[144:159]
	v_pk_add_f16 v148, v148, v149
	v_pk_add_f16 v150, v150, v151
	v_mfma_f32_32x32x16_f16 a[80:95], v[114:117], v[102:105], a[80:95]
	v_dot2c_f32_f16_e32 v134, 0x3c003c00, v148
	v_dot2c_f32_f16_e32 v135, 0x3c003c00, v150
	v_mfma_f32_32x32x16_f16 a[96:111], v[110:113], v[102:105], a[96:111]
	s_waitcnt lgkmcnt(0)
	v_mfma_f32_32x32x16_f16 a[0:15], v[18:21], v[74:77], a[0:15]
	s_load_dwordx16 s[68:83], s[30:31], 0x100
	s_load_dwordx16 s[52:67], s[30:31], 0x8100
	ds_read_b128 v[90:93], v145 offset:64
	ds_read_b128 v[82:85], v145 offset:2112
	v_mfma_f32_32x32x16_f16 a[240:255], v[38:41], v[74:77], a[240:255]
	ds_read_b128 v[50:53], v3
	v_pk_mul_f16 v148, v46, v136
	v_pk_mul_f16 v149, v42, v137
	v_pk_mul_f16 v150, v47, v136
	v_pk_mul_f16 v151, v43, v137
	v_mfma_f32_32x32x16_f16 a[16:31], v[18:21], v[126:129], a[16:31]
	ds_read_b128 v[54:57], v3 offset:4096
	v_pk_mul_f16 v152, v48, v136
	v_pk_mul_f16 v153, v44, v137
	v_pk_mul_f16 v154, v49, v136
	v_pk_mul_f16 v155, v45, v137
	v_mfma_f32_32x32x16_f16 a[224:239], v[38:41], v[126:129], a[224:239]
	ds_read_b128 v[58:61], v3 offset:8192
	v_pk_mul_f16 v156, v46, v140
	v_pk_mul_f16 v157, v42, v139
	v_pk_mul_f16 v158, v47, v140
	v_pk_mul_f16 v159, v43, v139
	v_mfma_f32_32x32x16_f16 a[32:47], v[18:21], v[122:125], a[32:47]
	ds_read_b128 v[62:65], v3 offset:12288
	v_pk_mul_f16 v160, v48, v140
	v_pk_mul_f16 v161, v44, v139
	v_pk_mul_f16 v162, v49, v140
	v_pk_mul_f16 v163, v45, v139
	v_mfma_f32_32x32x16_f16 a[208:223], v[38:41], v[122:125], a[208:223]
	ds_read_b128 v[66:69], v3 offset:16384
	v_pk_max_f16 v148, v148, v149
	v_pk_max_f16 v150, v150, v151
	v_pk_max_f16 v152, v152, v153
	v_pk_max_f16 v154, v154, v155
	v_mfma_f32_32x32x16_f16 a[48:63], v[18:21], v[118:121], a[48:63]
	ds_read_b128 v[70:73], v3 offset:20480
	v_pk_max_f16 v156, v156, v157
	v_pk_max_f16 v158, v158, v159
	v_pk_max_f16 v160, v160, v161
	v_pk_max_f16 v162, v162, v163
	v_mfma_f32_32x32x16_f16 a[192:207], v[38:41], v[118:121], a[192:207]
	ds_read_b128 v[78:81], v3 offset:24576
	v_cndmask_b32_e64 v114, v1, v148, s[36:37]
	s_mov_b64 vcc, s[38:39]
	v_cndmask_b32_sdwa v114, v1, v148, vcc dst_sel:WORD_1 dst_unused:UNUSED_PRESERVE src0_sel:WORD_1 src1_sel:WORD_1
	v_cndmask_b32_e64 v115, v1, v150, s[40:41]
	s_mov_b64 vcc, s[42:43]
	v_cndmask_b32_sdwa v115, v1, v150, vcc dst_sel:WORD_1 dst_unused:UNUSED_PRESERVE src0_sel:WORD_1 src1_sel:WORD_1
	v_mfma_f32_32x32x16_f16 a[64:79], v[18:21], v[106:109], a[64:79]
	ds_read_b128 v[102:105], v3 offset:28672
	v_cndmask_b32_e64 v116, v1, v152, s[44:45]
	s_mov_b64 vcc, s[46:47]
	v_cndmask_b32_sdwa v116, v1, v152, vcc dst_sel:WORD_1 dst_unused:UNUSED_PRESERVE src0_sel:WORD_1 src1_sel:WORD_1
	v_cndmask_b32_e64 v117, v1, v154, s[48:49]
	s_mov_b64 vcc, s[50:51]
	v_cndmask_b32_sdwa v117, v1, v154, vcc dst_sel:WORD_1 dst_unused:UNUSED_PRESERVE src0_sel:WORD_1 src1_sel:WORD_1
	v_mfma_f32_32x32x16_f16 a[176:191], v[38:41], v[106:109], a[176:191]
	v_cndmask_b32_e64 v110, v138, v156, s[4:5]
	s_mov_b64 vcc, s[6:7]
	v_cndmask_b32_sdwa v110, v138, v156, vcc dst_sel:WORD_1 dst_unused:UNUSED_PRESERVE src0_sel:WORD_1 src1_sel:WORD_1
	v_cndmask_b32_e64 v111, v138, v158, s[8:9]
	s_mov_b64 vcc, s[10:11]
	v_cndmask_b32_sdwa v111, v138, v158, vcc dst_sel:WORD_1 dst_unused:UNUSED_PRESERVE src0_sel:WORD_1 src1_sel:WORD_1
	v_mfma_f32_32x32x16_f16 a[112:127], v[18:21], v[98:101], a[112:127]
	v_cndmask_b32_e64 v112, v138, v160, s[12:13]
	s_mov_b64 vcc, s[14:15]
	v_cndmask_b32_sdwa v112, v138, v160, vcc dst_sel:WORD_1 dst_unused:UNUSED_PRESERVE src0_sel:WORD_1 src1_sel:WORD_1
	v_cndmask_b32_e64 v113, v138, v162, s[16:17]
	s_mov_b64 vcc, s[18:19]
	v_cndmask_b32_sdwa v113, v138, v162, vcc dst_sel:WORD_1 dst_unused:UNUSED_PRESERVE src0_sel:WORD_1 src1_sel:WORD_1
	v_mfma_f32_32x32x16_f16 a[160:175], v[38:41], v[98:101], a[160:175]
	v_pk_add_f16 v148, v115, v114
	v_pk_add_f16 v149, v116, v117
	v_mfma_f32_32x32x16_f16 a[128:143], v[18:21], v[94:97], a[128:143]
	v_pk_add_f16 v150, v111, v110
	v_pk_add_f16 v151, v112, v113
	v_mfma_f32_32x32x16_f16 a[144:159], v[38:41], v[94:97], a[144:159]
	v_pk_add_f16 v148, v148, v149
	v_pk_add_f16 v150, v150, v151
	v_mfma_f32_32x32x16_f16 a[80:95], v[18:21], v[86:89], a[80:95]
	v_dot2c_f32_f16_e32 v134, 0x3c003c00, v148
	v_dot2c_f32_f16_e32 v135, 0x3c003c00, v150
	v_mfma_f32_32x32x16_f16 a[96:111], v[38:41], v[86:89], a[96:111]
	s_waitcnt lgkmcnt(0)
	v_mfma_f32_32x32x16_f16 a[0:15], v[114:117], v[50:53], a[0:15]
	s_load_dwordx16 s[36:51], s[30:31], 0x140
	s_load_dwordx16 s[4:19], s[30:31], 0x8140
	ds_read_b128 v[46:49], v145 offset:96
	ds_read_b128 v[42:45], v145 offset:2144
	v_mfma_f32_32x32x16_f16 a[240:255], v[110:113], v[50:53], a[240:255]
	ds_read_b128 v[74:77], v146
	v_pk_mul_f16 v148, v90, v136
	v_pk_mul_f16 v149, v82, v137
	v_pk_mul_f16 v150, v91, v136
	v_pk_mul_f16 v151, v83, v137
	v_mfma_f32_32x32x16_f16 a[16:31], v[114:117], v[54:57], a[16:31]
	ds_read_b128 v[126:129], v146 offset:4096
	v_pk_mul_f16 v152, v92, v136
	v_pk_mul_f16 v153, v84, v137
	v_pk_mul_f16 v154, v93, v136
	v_pk_mul_f16 v155, v85, v137
	v_mfma_f32_32x32x16_f16 a[224:239], v[110:113], v[54:57], a[224:239]
	ds_read_b128 v[122:125], v146 offset:8192
	v_pk_mul_f16 v156, v90, v140
	v_pk_mul_f16 v157, v82, v139
	v_pk_mul_f16 v158, v91, v140
	v_pk_mul_f16 v159, v83, v139
	v_mfma_f32_32x32x16_f16 a[32:47], v[114:117], v[58:61], a[32:47]
	ds_read_b128 v[118:121], v146 offset:12288
	v_pk_mul_f16 v160, v92, v140
	v_pk_mul_f16 v161, v84, v139
	v_pk_mul_f16 v162, v93, v140
	v_pk_mul_f16 v163, v85, v139
	v_mfma_f32_32x32x16_f16 a[208:223], v[110:113], v[58:61], a[208:223]
	ds_read_b128 v[106:109], v146 offset:16384
	v_pk_max_f16 v148, v148, v149
	v_pk_max_f16 v150, v150, v151
	v_pk_max_f16 v152, v152, v153
	v_pk_max_f16 v154, v154, v155
	v_mfma_f32_32x32x16_f16 a[48:63], v[114:117], v[62:65], a[48:63]
	ds_read_b128 v[98:101], v146 offset:20480
	v_pk_max_f16 v156, v156, v157
	v_pk_max_f16 v158, v158, v159
	v_pk_max_f16 v160, v160, v161
	v_pk_max_f16 v162, v162, v163
	v_mfma_f32_32x32x16_f16 a[192:207], v[110:113], v[62:65], a[192:207]
	ds_read_b128 v[94:97], v146 offset:24576
	v_cndmask_b32_e64 v18, v1, v148, s[68:69]
	s_mov_b64 vcc, s[70:71]
	v_cndmask_b32_sdwa v18, v1, v148, vcc dst_sel:WORD_1 dst_unused:UNUSED_PRESERVE src0_sel:WORD_1 src1_sel:WORD_1
	v_cndmask_b32_e64 v19, v1, v150, s[72:73]
	s_mov_b64 vcc, s[74:75]
	v_cndmask_b32_sdwa v19, v1, v150, vcc dst_sel:WORD_1 dst_unused:UNUSED_PRESERVE src0_sel:WORD_1 src1_sel:WORD_1
	v_mfma_f32_32x32x16_f16 a[64:79], v[114:117], v[66:69], a[64:79]
	ds_read_b128 v[86:89], v146 offset:28672
	v_cndmask_b32_e64 v20, v1, v152, s[76:77]
	s_mov_b64 vcc, s[78:79]
	v_cndmask_b32_sdwa v20, v1, v152, vcc dst_sel:WORD_1 dst_unused:UNUSED_PRESERVE src0_sel:WORD_1 src1_sel:WORD_1
	v_cndmask_b32_e64 v21, v1, v154, s[80:81]
	s_mov_b64 vcc, s[82:83]
	v_cndmask_b32_sdwa v21, v1, v154, vcc dst_sel:WORD_1 dst_unused:UNUSED_PRESERVE src0_sel:WORD_1 src1_sel:WORD_1
	v_mfma_f32_32x32x16_f16 a[176:191], v[110:113], v[66:69], a[176:191]
	v_cndmask_b32_e64 v38, v138, v156, s[52:53]
	s_mov_b64 vcc, s[54:55]
	v_cndmask_b32_sdwa v38, v138, v156, vcc dst_sel:WORD_1 dst_unused:UNUSED_PRESERVE src0_sel:WORD_1 src1_sel:WORD_1
	v_cndmask_b32_e64 v39, v138, v158, s[56:57]
	s_mov_b64 vcc, s[58:59]
	v_cndmask_b32_sdwa v39, v138, v158, vcc dst_sel:WORD_1 dst_unused:UNUSED_PRESERVE src0_sel:WORD_1 src1_sel:WORD_1
	v_mfma_f32_32x32x16_f16 a[112:127], v[114:117], v[70:73], a[112:127]
	v_cndmask_b32_e64 v40, v138, v160, s[60:61]
	s_mov_b64 vcc, s[62:63]
	v_cndmask_b32_sdwa v40, v138, v160, vcc dst_sel:WORD_1 dst_unused:UNUSED_PRESERVE src0_sel:WORD_1 src1_sel:WORD_1
	v_cndmask_b32_e64 v41, v138, v162, s[64:65]
	s_mov_b64 vcc, s[66:67]
	v_cndmask_b32_sdwa v41, v138, v162, vcc dst_sel:WORD_1 dst_unused:UNUSED_PRESERVE src0_sel:WORD_1 src1_sel:WORD_1
	v_mfma_f32_32x32x16_f16 a[160:175], v[110:113], v[70:73], a[160:175]
	v_pk_add_f16 v148, v19, v18
	v_pk_add_f16 v149, v20, v21
	v_mfma_f32_32x32x16_f16 a[128:143], v[114:117], v[78:81], a[128:143]
	v_pk_add_f16 v150, v39, v38
	v_pk_add_f16 v151, v40, v41
	v_mfma_f32_32x32x16_f16 a[144:159], v[110:113], v[78:81], a[144:159]
	v_pk_add_f16 v148, v148, v149
	v_pk_add_f16 v150, v150, v151
	v_mfma_f32_32x32x16_f16 a[80:95], v[114:117], v[102:105], a[80:95]
	v_dot2c_f32_f16_e32 v134, 0x3c003c00, v148
	v_dot2c_f32_f16_e32 v135, 0x3c003c00, v150
	v_mfma_f32_32x32x16_f16 a[96:111], v[110:113], v[102:105], a[96:111]
	s_add_i32 s92, s92, 0x9000
	s_cmp_lg_u32 s91, 2
	s_cselect_b32 s30, s92, 0
	s_add_u32 s20, s20, 0x100
	s_addc_u32 s21, s21, 0
	s_add_u32 s94, s94, 0x8000
	s_addc_u32 s95, s95, 0
	v_add_u32_e32 v145, 0x80, v145
	s_cmpk_eq_i32 s20, 0xf00
	s_mov_b32 s30, s91
	s_waitcnt vmcnt(0)
	s_waitcnt lgkmcnt(0)
	s_barrier
	s_cbranch_scc0 .LBB1_3
	s_waitcnt lgkmcnt(0)
	v_mfma_f32_32x32x16_f16 a[0:15], v[18:21], v[74:77], a[0:15]
	s_load_dwordx16 s[68:83], s[0:1], 0xf80
	s_load_dwordx16 s[52:67], s[0:1], 0x8f80
	ds_read_b128 v[90:93], v142 offset:1984
	ds_read_b128 v[82:85], v142 offset:4032
	v_mfma_f32_32x32x16_f16 a[240:255], v[38:41], v[74:77], a[240:255]
	ds_read_b128 v[50:53], v208
	v_pk_mul_f16 v148, v46, v136
	v_pk_mul_f16 v149, v42, v137
	v_pk_mul_f16 v150, v47, v136
	v_pk_mul_f16 v151, v43, v137
	v_mfma_f32_32x32x16_f16 a[16:31], v[18:21], v[126:129], a[16:31]
	ds_read_b128 v[54:57], v208 offset:4096
	v_pk_mul_f16 v152, v48, v136
	v_pk_mul_f16 v153, v44, v137
	v_pk_mul_f16 v154, v49, v136
	v_pk_mul_f16 v155, v45, v137
	v_mfma_f32_32x32x16_f16 a[224:239], v[38:41], v[126:129], a[224:239]
	ds_read_b128 v[58:61], v208 offset:8192
	v_pk_mul_f16 v156, v46, v140
	v_pk_mul_f16 v157, v42, v139
	v_pk_mul_f16 v158, v47, v140
	v_pk_mul_f16 v159, v43, v139
	v_mfma_f32_32x32x16_f16 a[32:47], v[18:21], v[122:125], a[32:47]
	ds_read_b128 v[62:65], v208 offset:12288
	v_pk_mul_f16 v160, v48, v140
	v_pk_mul_f16 v161, v44, v139
	v_pk_mul_f16 v162, v49, v140
	v_pk_mul_f16 v163, v45, v139
	v_mfma_f32_32x32x16_f16 a[208:223], v[38:41], v[122:125], a[208:223]
	ds_read_b128 v[66:69], v208 offset:16384
	v_pk_max_f16 v148, v148, v149
	v_pk_max_f16 v150, v150, v151
	v_pk_max_f16 v152, v152, v153
	v_pk_max_f16 v154, v154, v155
	v_mfma_f32_32x32x16_f16 a[48:63], v[18:21], v[118:121], a[48:63]
	ds_read_b128 v[70:73], v208 offset:20480
	v_pk_max_f16 v156, v156, v157
	v_pk_max_f16 v158, v158, v159
	v_pk_max_f16 v160, v160, v161
	v_pk_max_f16 v162, v162, v163
	v_mfma_f32_32x32x16_f16 a[192:207], v[38:41], v[118:121], a[192:207]
	ds_read_b128 v[78:81], v208 offset:24576
	v_cndmask_b32_e64 v114, v1, v148, s[36:37]
	s_mov_b64 vcc, s[38:39]
	v_cndmask_b32_sdwa v114, v1, v148, vcc dst_sel:WORD_1 dst_unused:UNUSED_PRESERVE src0_sel:WORD_1 src1_sel:WORD_1
	v_cndmask_b32_e64 v115, v1, v150, s[40:41]
	s_mov_b64 vcc, s[42:43]
	v_cndmask_b32_sdwa v115, v1, v150, vcc dst_sel:WORD_1 dst_unused:UNUSED_PRESERVE src0_sel:WORD_1 src1_sel:WORD_1
	v_mfma_f32_32x32x16_f16 a[64:79], v[18:21], v[106:109], a[64:79]
	ds_read_b128 v[102:105], v208 offset:28672
	v_cndmask_b32_e64 v116, v1, v152, s[44:45]
	s_mov_b64 vcc, s[46:47]
	v_cndmask_b32_sdwa v116, v1, v152, vcc dst_sel:WORD_1 dst_unused:UNUSED_PRESERVE src0_sel:WORD_1 src1_sel:WORD_1
	v_cndmask_b32_e64 v117, v1, v154, s[48:49]
	s_mov_b64 vcc, s[50:51]
	v_cndmask_b32_sdwa v117, v1, v154, vcc dst_sel:WORD_1 dst_unused:UNUSED_PRESERVE src0_sel:WORD_1 src1_sel:WORD_1
	v_mfma_f32_32x32x16_f16 a[176:191], v[38:41], v[106:109], a[176:191]
	v_cndmask_b32_e64 v110, v138, v156, s[4:5]
	s_mov_b64 vcc, s[6:7]
	v_cndmask_b32_sdwa v110, v138, v156, vcc dst_sel:WORD_1 dst_unused:UNUSED_PRESERVE src0_sel:WORD_1 src1_sel:WORD_1
	v_cndmask_b32_e64 v111, v138, v158, s[8:9]
	s_mov_b64 vcc, s[10:11]
	v_cndmask_b32_sdwa v111, v138, v158, vcc dst_sel:WORD_1 dst_unused:UNUSED_PRESERVE src0_sel:WORD_1 src1_sel:WORD_1
	v_mfma_f32_32x32x16_f16 a[112:127], v[18:21], v[98:101], a[112:127]
	v_cndmask_b32_e64 v112, v138, v160, s[12:13]
	s_mov_b64 vcc, s[14:15]
	v_cndmask_b32_sdwa v112, v138, v160, vcc dst_sel:WORD_1 dst_unused:UNUSED_PRESERVE src0_sel:WORD_1 src1_sel:WORD_1
	v_cndmask_b32_e64 v113, v138, v162, s[16:17]
	s_mov_b64 vcc, s[18:19]
	v_cndmask_b32_sdwa v113, v138, v162, vcc dst_sel:WORD_1 dst_unused:UNUSED_PRESERVE src0_sel:WORD_1 src1_sel:WORD_1
	v_mfma_f32_32x32x16_f16 a[160:175], v[38:41], v[98:101], a[160:175]
	v_pk_add_f16 v148, v115, v114
	v_pk_add_f16 v149, v116, v117
	v_mfma_f32_32x32x16_f16 a[128:143], v[18:21], v[94:97], a[128:143]
	v_pk_add_f16 v150, v111, v110
	v_pk_add_f16 v151, v112, v113
	v_mfma_f32_32x32x16_f16 a[144:159], v[38:41], v[94:97], a[144:159]
	v_pk_add_f16 v148, v148, v149
	v_pk_add_f16 v150, v150, v151
	v_mfma_f32_32x32x16_f16 a[80:95], v[18:21], v[86:89], a[80:95]
	v_dot2c_f32_f16_e32 v134, 0x3c003c00, v148
	v_dot2c_f32_f16_e32 v135, 0x3c003c00, v150
	v_mfma_f32_32x32x16_f16 a[96:111], v[38:41], v[86:89], a[96:111]
	s_waitcnt lgkmcnt(0)
	v_mfma_f32_32x32x16_f16 a[0:15], v[114:117], v[50:53], a[0:15]
	s_load_dwordx16 s[36:51], s[0:1], 0xfc0
	s_load_dwordx16 s[4:19], s[0:1], 0x8fc0
	ds_read_b128 v[46:49], v142 offset:2016
	ds_read_b128 v[42:45], v142 offset:4064
	v_mfma_f32_32x32x16_f16 a[240:255], v[110:113], v[50:53], a[240:255]
	ds_read_b128 v[74:77], v209
	v_pk_mul_f16 v148, v90, v136
	v_pk_mul_f16 v149, v82, v137
	v_pk_mul_f16 v150, v91, v136
	v_pk_mul_f16 v151, v83, v137
	v_mfma_f32_32x32x16_f16 a[16:31], v[114:117], v[54:57], a[16:31]
	ds_read_b128 v[126:129], v209 offset:4096
	v_pk_mul_f16 v152, v92, v136
	v_pk_mul_f16 v153, v84, v137
	v_pk_mul_f16 v154, v93, v136
	v_pk_mul_f16 v155, v85, v137
	v_mfma_f32_32x32x16_f16 a[224:239], v[110:113], v[54:57], a[224:239]
	ds_read_b128 v[122:125], v209 offset:8192
	v_pk_mul_f16 v156, v90, v140
	v_pk_mul_f16 v157, v82, v139
	v_pk_mul_f16 v158, v91, v140
	v_pk_mul_f16 v159, v83, v139
	v_mfma_f32_32x32x16_f16 a[32:47], v[114:117], v[58:61], a[32:47]
	ds_read_b128 v[118:121], v209 offset:12288
	v_pk_mul_f16 v160, v92, v140
	v_pk_mul_f16 v161, v84, v139
	v_pk_mul_f16 v162, v93, v140
	v_pk_mul_f16 v163, v85, v139
	v_mfma_f32_32x32x16_f16 a[208:223], v[110:113], v[58:61], a[208:223]
	ds_read_b128 v[106:109], v209 offset:16384
	v_pk_max_f16 v148, v148, v149
	v_pk_max_f16 v150, v150, v151
	v_pk_max_f16 v152, v152, v153
	v_pk_max_f16 v154, v154, v155
	v_mfma_f32_32x32x16_f16 a[48:63], v[114:117], v[62:65], a[48:63]
	ds_read_b128 v[98:101], v209 offset:20480
	v_pk_max_f16 v156, v156, v157
	v_pk_max_f16 v158, v158, v159
	v_pk_max_f16 v160, v160, v161
	v_pk_max_f16 v162, v162, v163
	v_mfma_f32_32x32x16_f16 a[192:207], v[110:113], v[62:65], a[192:207]
	ds_read_b128 v[94:97], v209 offset:24576
	v_cndmask_b32_e64 v18, v1, v148, s[68:69]
	s_mov_b64 vcc, s[70:71]
	v_cndmask_b32_sdwa v18, v1, v148, vcc dst_sel:WORD_1 dst_unused:UNUSED_PRESERVE src0_sel:WORD_1 src1_sel:WORD_1
	v_cndmask_b32_e64 v19, v1, v150, s[72:73]
	s_mov_b64 vcc, s[74:75]
	v_cndmask_b32_sdwa v19, v1, v150, vcc dst_sel:WORD_1 dst_unused:UNUSED_PRESERVE src0_sel:WORD_1 src1_sel:WORD_1
	v_mfma_f32_32x32x16_f16 a[64:79], v[114:117], v[66:69], a[64:79]
	ds_read_b128 v[86:89], v209 offset:28672
	v_cndmask_b32_e64 v20, v1, v152, s[76:77]
	s_mov_b64 vcc, s[78:79]
	v_cndmask_b32_sdwa v20, v1, v152, vcc dst_sel:WORD_1 dst_unused:UNUSED_PRESERVE src0_sel:WORD_1 src1_sel:WORD_1
	v_cndmask_b32_e64 v21, v1, v154, s[80:81]
	s_mov_b64 vcc, s[82:83]
	v_cndmask_b32_sdwa v21, v1, v154, vcc dst_sel:WORD_1 dst_unused:UNUSED_PRESERVE src0_sel:WORD_1 src1_sel:WORD_1
	v_mfma_f32_32x32x16_f16 a[176:191], v[110:113], v[66:69], a[176:191]
	v_cndmask_b32_e64 v38, v138, v156, s[52:53]
	s_mov_b64 vcc, s[54:55]
	v_cndmask_b32_sdwa v38, v138, v156, vcc dst_sel:WORD_1 dst_unused:UNUSED_PRESERVE src0_sel:WORD_1 src1_sel:WORD_1
	v_cndmask_b32_e64 v39, v138, v158, s[56:57]
	s_mov_b64 vcc, s[58:59]
	v_cndmask_b32_sdwa v39, v138, v158, vcc dst_sel:WORD_1 dst_unused:UNUSED_PRESERVE src0_sel:WORD_1 src1_sel:WORD_1
	v_mfma_f32_32x32x16_f16 a[112:127], v[114:117], v[70:73], a[112:127]
	v_cndmask_b32_e64 v40, v138, v160, s[60:61]
	s_mov_b64 vcc, s[62:63]
	v_cndmask_b32_sdwa v40, v138, v160, vcc dst_sel:WORD_1 dst_unused:UNUSED_PRESERVE src0_sel:WORD_1 src1_sel:WORD_1
	v_cndmask_b32_e64 v41, v138, v162, s[64:65]
	s_mov_b64 vcc, s[66:67]
	v_cndmask_b32_sdwa v41, v138, v162, vcc dst_sel:WORD_1 dst_unused:UNUSED_PRESERVE src0_sel:WORD_1 src1_sel:WORD_1
	v_mfma_f32_32x32x16_f16 a[160:175], v[110:113], v[70:73], a[160:175]
	v_pk_add_f16 v148, v19, v18
	v_pk_add_f16 v149, v20, v21
	v_mfma_f32_32x32x16_f16 a[128:143], v[114:117], v[78:81], a[128:143]
	v_pk_add_f16 v150, v39, v38
	v_pk_add_f16 v151, v40, v41
	v_mfma_f32_32x32x16_f16 a[144:159], v[110:113], v[78:81], a[144:159]
	v_pk_add_f16 v148, v148, v149
	v_pk_add_f16 v150, v150, v151
	v_mfma_f32_32x32x16_f16 a[80:95], v[114:117], v[102:105], a[80:95]
	v_dot2c_f32_f16_e32 v134, 0x3c003c00, v148
	v_dot2c_f32_f16_e32 v135, 0x3c003c00, v150
	v_mfma_f32_32x32x16_f16 a[96:111], v[110:113], v[102:105], a[96:111]
	s_waitcnt lgkmcnt(0)
	v_mfma_f32_32x32x16_f16 a[0:15], v[18:21], v[74:77], a[0:15]
	v_mfma_f32_32x32x16_f16 a[240:255], v[38:41], v[74:77], a[240:255]
	ds_read_b128 v[50:53], v210
	v_pk_mul_f16 v148, v46, v136
	v_pk_mul_f16 v149, v42, v137
	v_pk_mul_f16 v150, v47, v136
	v_pk_mul_f16 v151, v43, v137
	v_mfma_f32_32x32x16_f16 a[16:31], v[18:21], v[126:129], a[16:31]
	ds_read_b128 v[54:57], v210 offset:4096
	v_pk_mul_f16 v152, v48, v136
	v_pk_mul_f16 v153, v44, v137
	v_pk_mul_f16 v154, v49, v136
	v_pk_mul_f16 v155, v45, v137
	v_mfma_f32_32x32x16_f16 a[224:239], v[38:41], v[126:129], a[224:239]
	ds_read_b128 v[58:61], v210 offset:8192
	v_pk_mul_f16 v156, v46, v140
	v_pk_mul_f16 v157, v42, v139
	v_pk_mul_f16 v158, v47, v140
	v_pk_mul_f16 v159, v43, v139
	v_mfma_f32_32x32x16_f16 a[32:47], v[18:21], v[122:125], a[32:47]
	ds_read_b128 v[62:65], v210 offset:12288
	v_pk_mul_f16 v160, v48, v140
	v_pk_mul_f16 v161, v44, v139
	v_pk_mul_f16 v162, v49, v140
	v_pk_mul_f16 v163, v45, v139
	v_mfma_f32_32x32x16_f16 a[208:223], v[38:41], v[122:125], a[208:223]
	ds_read_b128 v[66:69], v210 offset:16384
	v_pk_max_f16 v148, v148, v149
	v_pk_max_f16 v150, v150, v151
	v_pk_max_f16 v152, v152, v153
	v_pk_max_f16 v154, v154, v155
	v_mfma_f32_32x32x16_f16 a[48:63], v[18:21], v[118:121], a[48:63]
	ds_read_b128 v[70:73], v210 offset:20480
	v_pk_max_f16 v156, v156, v157
	v_pk_max_f16 v158, v158, v159
	v_pk_max_f16 v160, v160, v161
	v_pk_max_f16 v162, v162, v163
	v_mfma_f32_32x32x16_f16 a[192:207], v[38:41], v[118:121], a[192:207]
	ds_read_b128 v[78:81], v210 offset:24576
	v_cndmask_b32_e64 v114, v1, v148, s[36:37]
	s_mov_b64 vcc, s[38:39]
	v_cndmask_b32_sdwa v114, v1, v148, vcc dst_sel:WORD_1 dst_unused:UNUSED_PRESERVE src0_sel:WORD_1 src1_sel:WORD_1
	v_cndmask_b32_e64 v115, v1, v150, s[40:41]
	s_mov_b64 vcc, s[42:43]
	v_cndmask_b32_sdwa v115, v1, v150, vcc dst_sel:WORD_1 dst_unused:UNUSED_PRESERVE src0_sel:WORD_1 src1_sel:WORD_1
	v_mfma_f32_32x32x16_f16 a[64:79], v[18:21], v[106:109], a[64:79]
	ds_read_b128 v[102:105], v210 offset:28672
	v_cndmask_b32_e64 v116, v1, v152, s[44:45]
	s_mov_b64 vcc, s[46:47]
	v_cndmask_b32_sdwa v116, v1, v152, vcc dst_sel:WORD_1 dst_unused:UNUSED_PRESERVE src0_sel:WORD_1 src1_sel:WORD_1
	v_cndmask_b32_e64 v117, v1, v154, s[48:49]
	s_mov_b64 vcc, s[50:51]
	v_cndmask_b32_sdwa v117, v1, v154, vcc dst_sel:WORD_1 dst_unused:UNUSED_PRESERVE src0_sel:WORD_1 src1_sel:WORD_1
	v_mfma_f32_32x32x16_f16 a[176:191], v[38:41], v[106:109], a[176:191]
	v_cndmask_b32_e64 v110, v138, v156, s[4:5]
	s_mov_b64 vcc, s[6:7]
	v_cndmask_b32_sdwa v110, v138, v156, vcc dst_sel:WORD_1 dst_unused:UNUSED_PRESERVE src0_sel:WORD_1 src1_sel:WORD_1
	v_cndmask_b32_e64 v111, v138, v158, s[8:9]
	s_mov_b64 vcc, s[10:11]
	v_cndmask_b32_sdwa v111, v138, v158, vcc dst_sel:WORD_1 dst_unused:UNUSED_PRESERVE src0_sel:WORD_1 src1_sel:WORD_1
	v_mfma_f32_32x32x16_f16 a[112:127], v[18:21], v[98:101], a[112:127]
	v_cndmask_b32_e64 v112, v138, v160, s[12:13]
	s_mov_b64 vcc, s[14:15]
	v_cndmask_b32_sdwa v112, v138, v160, vcc dst_sel:WORD_1 dst_unused:UNUSED_PRESERVE src0_sel:WORD_1 src1_sel:WORD_1
	v_cndmask_b32_e64 v113, v138, v162, s[16:17]
	s_mov_b64 vcc, s[18:19]
	v_cndmask_b32_sdwa v113, v138, v162, vcc dst_sel:WORD_1 dst_unused:UNUSED_PRESERVE src0_sel:WORD_1 src1_sel:WORD_1
	v_mfma_f32_32x32x16_f16 a[160:175], v[38:41], v[98:101], a[160:175]
	v_pk_add_f16 v148, v115, v114
	v_pk_add_f16 v149, v116, v117
	v_mfma_f32_32x32x16_f16 a[128:143], v[18:21], v[94:97], a[128:143]
	v_pk_add_f16 v150, v111, v110
	v_pk_add_f16 v151, v112, v113
	v_mfma_f32_32x32x16_f16 a[144:159], v[38:41], v[94:97], a[144:159]
	v_pk_add_f16 v148, v148, v149
	v_pk_add_f16 v150, v150, v151
	v_mfma_f32_32x32x16_f16 a[80:95], v[18:21], v[86:89], a[80:95]
	v_dot2c_f32_f16_e32 v134, 0x3c003c00, v148
	v_dot2c_f32_f16_e32 v135, 0x3c003c00, v150
	v_mfma_f32_32x32x16_f16 a[96:111], v[38:41], v[86:89], a[96:111]
	s_waitcnt lgkmcnt(0)
	v_mfma_f32_32x32x16_f16 a[0:15], v[114:117], v[50:53], a[0:15]
	v_mfma_f32_32x32x16_f16 a[240:255], v[110:113], v[50:53], a[240:255]
	v_mfma_f32_32x32x16_f16 a[16:31], v[114:117], v[54:57], a[16:31]
	v_mfma_f32_32x32x16_f16 a[224:239], v[110:113], v[54:57], a[224:239]
	v_mfma_f32_32x32x16_f16 a[32:47], v[114:117], v[58:61], a[32:47]
	v_mfma_f32_32x32x16_f16 a[208:223], v[110:113], v[58:61], a[208:223]
	v_mfma_f32_32x32x16_f16 a[48:63], v[114:117], v[62:65], a[48:63]
	v_mfma_f32_32x32x16_f16 a[192:207], v[110:113], v[62:65], a[192:207]
	v_mfma_f32_32x32x16_f16 a[64:79], v[114:117], v[66:69], a[64:79]
	v_mfma_f32_32x32x16_f16 a[176:191], v[110:113], v[66:69], a[176:191]
	v_mfma_f32_32x32x16_f16 a[112:127], v[114:117], v[70:73], a[112:127]
	v_mfma_f32_32x32x16_f16 a[160:175], v[110:113], v[70:73], a[160:175]
	v_mfma_f32_32x32x16_f16 a[128:143], v[114:117], v[78:81], a[128:143]
	v_mfma_f32_32x32x16_f16 a[144:159], v[110:113], v[78:81], a[144:159]
	v_mfma_f32_32x32x16_f16 a[80:95], v[114:117], v[102:105], a[80:95]
	v_mfma_f32_32x32x16_f16 a[96:111], v[110:113], v[102:105], a[96:111]
	v_readfirstlane_b32 s1, v0
	s_and_b32 s0, s3, 0xffffff00
	s_andn2_b32 s1, s1, 63
	s_add_i32 s4, s1, s0
	s_lshl_b32 s0, s2, 13
	s_and_b32 s6, s0, 0xe000
	s_ashr_i32 s5, s4, 31
	s_add_u32 s0, s4, s6
	s_addc_u32 s1, s5, 0
	s_lshl_b64 s[2:3], s[0:1], 9
	v_lshrrev_b32_e32 v0, 3, v132
	s_add_u32 s2, s22, s2
	v_and_b32_e32 v3, 12, v0
	s_addc_u32 s3, s23, s3
	v_lshlrev_b32_e32 v0, 9, v3
	v_mov_b32_e32 v1, 0
	v_lshl_add_u64 v[4:5], s[2:3], 0, v[0:1]
	v_lshlrev_b32_e32 v0, 4, v132
	v_and_b32_e32 v0, 0x1f0, v0
	v_lshl_add_u64 v[4:5], v[4:5], 0, v[0:1]
	v_accvgpr_read_b32 v6, a0
	v_accvgpr_read_b32 v7, a16
	v_accvgpr_read_b32 v8, a32
	v_max3_f32 v0, |v6|, |v7|, |v8|
	v_accvgpr_read_b32 v9, a48
	v_accvgpr_read_b32 v14, a64
	v_max3_f32 v0, |v0|, |v9|, |v14|
	v_accvgpr_read_b32 v15, a112
	v_accvgpr_read_b32 v16, a128
	v_max3_f32 v0, |v0|, |v15|, |v16|
	v_accvgpr_read_b32 v17, a80
	v_max3_f32 v10, |v0|, |v17|, |v17|
	v_accvgpr_read_b32 v18, a1
	v_accvgpr_read_b32 v19, a17
	v_accvgpr_read_b32 v20, a33
	v_max3_f32 v0, |v18|, |v19|, |v20|
	v_accvgpr_read_b32 v21, a49
	v_accvgpr_read_b32 v22, a65
	v_max3_f32 v0, |v0|, |v21|, |v22|
	v_accvgpr_read_b32 v23, a113
	v_accvgpr_read_b32 v24, a129
	v_max3_f32 v0, |v0|, |v23|, |v24|
	v_accvgpr_read_b32 v25, a81
	v_max3_f32 v11, |v0|, |v25|, |v25|
	v_accvgpr_read_b32 v26, a2
	v_accvgpr_read_b32 v27, a18
	v_accvgpr_read_b32 v28, a34
	v_max3_f32 v0, |v26|, |v27|, |v28|
	v_accvgpr_read_b32 v29, a50
	v_accvgpr_read_b32 v30, a66
	v_max3_f32 v0, |v0|, |v29|, |v30|
	v_accvgpr_read_b32 v31, a114
	v_accvgpr_read_b32 v32, a130
	v_max3_f32 v0, |v0|, |v31|, |v32|
	v_accvgpr_read_b32 v33, a82
	v_max3_f32 v12, |v0|, |v33|, |v33|
	v_accvgpr_read_b32 v34, a3
	v_accvgpr_read_b32 v35, a19
	v_accvgpr_read_b32 v36, a35
	v_max3_f32 v0, |v34|, |v35|, |v36|
	v_accvgpr_read_b32 v37, a51
	v_accvgpr_read_b32 v38, a67
	v_max3_f32 v0, |v0|, |v37|, |v38|
	v_accvgpr_read_b32 v39, a115
	v_accvgpr_read_b32 v40, a131
	v_max3_f32 v0, |v0|, |v39|, |v40|
	v_accvgpr_read_b32 v41, a83
	v_max3_f32 v13, |v0|, |v41|, |v41|
	v_lshlrev_b32_e32 v0, 2, v3
	s_nop 1
	v_max_f32_dpp v10, v10, v10 quad_perm:[1,0,3,2] row_mask:0xf bank_mask:0xf
	v_max_f32_dpp v11, v11, v11 quad_perm:[1,0,3,2] row_mask:0xf bank_mask:0xf
	v_max_f32_dpp v12, v12, v12 quad_perm:[1,0,3,2] row_mask:0xf bank_mask:0xf
	v_max_f32_dpp v13, v13, v13 quad_perm:[1,0,3,2] row_mask:0xf bank_mask:0xf
	v_max_f32_dpp v10, v10, v10 quad_perm:[2,3,0,1] row_mask:0xf bank_mask:0xf
	v_max_f32_dpp v11, v11, v11 quad_perm:[2,3,0,1] row_mask:0xf bank_mask:0xf
	v_max_f32_dpp v12, v12, v12 quad_perm:[2,3,0,1] row_mask:0xf bank_mask:0xf
	v_max_f32_dpp v13, v13, v13 quad_perm:[2,3,0,1] row_mask:0xf bank_mask:0xf
	v_max_f32_dpp v10, v10, v10 row_half_mirror row_mask:0xf bank_mask:0xf
	v_max_f32_dpp v11, v11, v11 row_half_mirror row_mask:0xf bank_mask:0xf
	v_max_f32_dpp v12, v12, v12 row_half_mirror row_mask:0xf bank_mask:0xf
	v_max_f32_dpp v13, v13, v13 row_half_mirror row_mask:0xf bank_mask:0xf
	v_max_f32_dpp v10, v10, v10 row_mirror row_mask:0xf bank_mask:0xf
	v_max_f32_dpp v11, v11, v11 row_mirror row_mask:0xf bank_mask:0xf
	v_max_f32_dpp v12, v12, v12 row_mirror row_mask:0xf bank_mask:0xf
	v_max_f32_dpp v13, v13, v13 row_mirror row_mask:0xf bank_mask:0xf
	s_nop 0
	ds_swizzle_b32 v232, v10 offset:swizzle(SWAP,16)
	ds_swizzle_b32 v233, v12 offset:swizzle(SWAP,16)
	ds_swizzle_b32 v234, v11 offset:swizzle(SWAP,16)
	ds_swizzle_b32 v235, v13 offset:swizzle(SWAP,16)
	s_waitcnt lgkmcnt(0)
	v_max_f32_e32 v10, v10, v232
	v_rcp_f32_e32 v42, v10
	v_cmp_lt_f32_e32 vcc, 0, v10
	s_waitcnt lgkmcnt(0)
	v_max_f32_e32 v12, v12, v233
	s_waitcnt lgkmcnt(0)
	v_max_f32_e32 v11, v11, v234
	s_lshl_b32 s2, s6, 2
	v_cndmask_b32_e32 v3, 0, v42, vcc
	v_pk_mul_f32 v[224:225], v[6:7], v[2:3] op_sel:[0,1] op_sel_hi:[1,1]
	v_pk_mul_f32 v[226:227], v[8:9], v[2:3] op_sel:[0,1] op_sel_hi:[1,1]
	v_cvt_pknorm_i16_f32 v6, v224, v225
	v_cvt_pknorm_i16_f32 v7, v226, v227
	v_pk_mul_f32 v[228:229], v[14:15], v[2:3] op_sel:[0,1] op_sel_hi:[1,1]
	v_rcp_f32_e32 v14, v11
	v_cvt_pknorm_i16_f32 v8, v228, v229
	v_pk_mul_f32 v[230:231], v[16:17], v[2:3] op_sel:[0,1] op_sel_hi:[1,1]
	v_cmp_lt_f32_e32 vcc, 0, v11
	v_cvt_pknorm_i16_f32 v9, v230, v231
	global_store_dwordx4 v[4:5], v[6:9], off sc0 sc1
	s_add_u32 s6, s24, s2
	v_cndmask_b32_e32 v3, 0, v14, vcc
	v_pk_mul_f32 v[224:225], v[18:19], v[2:3] op_sel:[0,1] op_sel_hi:[1,1]
	v_pk_mul_f32 v[226:227], v[20:21], v[2:3] op_sel:[0,1] op_sel_hi:[1,1]
	v_cvt_pknorm_i16_f32 v6, v224, v225
	v_cvt_pknorm_i16_f32 v7, v226, v227
	v_pk_mul_f32 v[228:229], v[22:23], v[2:3] op_sel:[0,1] op_sel_hi:[1,1]
	v_pk_mul_f32 v[230:231], v[24:25], v[2:3] op_sel:[0,1] op_sel_hi:[1,1]
	v_cvt_pknorm_i16_f32 v8, v228, v229
	v_cvt_pknorm_i16_f32 v9, v230, v231
	v_rcp_f32_e32 v3, v12
	s_addc_u32 s7, s25, 0
	s_lshl_b64 s[2:3], s[4:5], 2
	s_mov_b64 s[4:5], 0x200
	s_add_u32 s2, s6, s2
	v_lshl_add_u64 v[14:15], v[4:5], 0, s[4:5]
	s_mov_b32 s4, 0x38000100
	v_cmp_lt_f32_e32 vcc, 0, v12
	s_addc_u32 s3, s7, s3
	global_store_dwordx4 v[14:15], v[6:9], off sc0 sc1
	s_nop 1
	v_pk_mul_f32 v[6:7], v[10:11], s[4:5] op_sel_hi:[1,0]
	v_cndmask_b32_e32 v3, 0, v3, vcc
	global_store_dwordx2 v0, v[6:7], s[2:3]
	v_pk_mul_f32 v[224:225], v[26:27], v[2:3] op_sel:[0,1] op_sel_hi:[1,1]
	v_pk_mul_f32 v[226:227], v[28:29], v[2:3] op_sel:[0,1] op_sel_hi:[1,1]
	v_cvt_pknorm_i16_f32 v6, v224, v225
	v_cvt_pknorm_i16_f32 v7, v226, v227
	v_pk_mul_f32 v[228:229], v[30:31], v[2:3] op_sel:[0,1] op_sel_hi:[1,1]
	v_pk_mul_f32 v[230:231], v[32:33], v[2:3] op_sel:[0,1] op_sel_hi:[1,1]
	v_cvt_pknorm_i16_f32 v8, v228, v229
	s_waitcnt lgkmcnt(0)
	v_max_f32_e32 v13, v13, v235
	v_cvt_pknorm_i16_f32 v9, v230, v231
	v_rcp_f32_e32 v3, v13
	v_cmp_lt_f32_e32 vcc, 0, v13
	s_mov_b64 s[6:7], 0x400
	v_lshl_add_u64 v[10:11], v[4:5], 0, s[6:7]
	v_cndmask_b32_e32 v3, 0, v3, vcc
	global_store_dwordx4 v[10:11], v[6:9], off sc0 sc1
	v_pk_mul_f32 v[224:225], v[34:35], v[2:3] op_sel:[0,1] op_sel_hi:[1,1]
	v_pk_mul_f32 v[226:227], v[36:37], v[2:3] op_sel:[0,1] op_sel_hi:[1,1]
	v_cvt_pknorm_i16_f32 v6, v224, v225
	v_cvt_pknorm_i16_f32 v7, v226, v227
	v_pk_mul_f32 v[228:229], v[38:39], v[2:3] op_sel:[0,1] op_sel_hi:[1,1]
	v_pk_mul_f32 v[230:231], v[40:41], v[2:3] op_sel:[0,1] op_sel_hi:[1,1]
	v_cvt_pknorm_i16_f32 v8, v228, v229
	s_mov_b64 s[6:7], 0x600
	v_cvt_pknorm_i16_f32 v9, v230, v231
	v_lshl_add_u64 v[10:11], v[4:5], 0, s[6:7]
	global_store_dwordx4 v[10:11], v[6:9], off sc0 sc1
	s_nop 1
	v_pk_mul_f32 v[6:7], v[12:13], s[4:5] op_sel_hi:[1,0]
	v_lshlrev_b32_e32 v2, 2, v132
	global_store_dwordx2 v0, v[6:7], s[2:3] offset:8
	v_accvgpr_read_b32 v42, a4
	v_accvgpr_read_b32 v6, a20
	v_accvgpr_read_b32 v7, a36
	v_max3_f32 v8, |v42|, |v6|, |v7|
	v_accvgpr_read_b32 v9, a52
	v_accvgpr_read_b32 v14, a68
	v_max3_f32 v8, |v8|, |v9|, |v14|
	v_accvgpr_read_b32 v15, a116
	v_accvgpr_read_b32 v16, a132
	v_max3_f32 v8, |v8|, |v15|, |v16|
	v_accvgpr_read_b32 v10, a84
	v_accvgpr_read_b32 v43, a5
	v_accvgpr_read_b32 v17, a84
	v_max3_f32 v8, |v8|, |v17|, |v10|
	v_accvgpr_read_b32 v19, a21
	v_accvgpr_read_b32 v20, a37
	v_max3_f32 v10, |v43|, |v19|, |v20|
	v_accvgpr_read_b32 v21, a53
	v_accvgpr_read_b32 v22, a69
	v_max3_f32 v10, |v10|, |v21|, |v22|
	v_accvgpr_read_b32 v23, a117
	v_accvgpr_read_b32 v24, a133
	v_max3_f32 v10, |v10|, |v23|, |v24|
	v_accvgpr_read_b32 v44, a6
	v_accvgpr_read_b32 v25, a85
	v_max3_f32 v11, |v10|, |v25|, |v25|
	v_accvgpr_read_b32 v27, a22
	v_accvgpr_read_b32 v28, a38
	v_max3_f32 v10, |v44|, |v27|, |v28|
	v_accvgpr_read_b32 v29, a54
	v_accvgpr_read_b32 v30, a70
	v_max3_f32 v10, |v10|, |v29|, |v30|
	v_accvgpr_read_b32 v31, a118
	v_accvgpr_read_b32 v32, a134
	v_max3_f32 v10, |v10|, |v31|, |v32|
	v_accvgpr_read_b32 v45, a7
	v_accvgpr_read_b32 v33, a86
	v_max3_f32 v12, |v10|, |v33|, |v33|
	v_accvgpr_read_b32 v35, a23
	v_accvgpr_read_b32 v36, a39
	v_max3_f32 v10, |v45|, |v35|, |v36|
	v_accvgpr_read_b32 v37, a55
	v_accvgpr_read_b32 v38, a71
	v_max3_f32 v10, |v10|, |v37|, |v38|
	v_accvgpr_read_b32 v39, a119
	v_accvgpr_read_b32 v40, a135
	v_max3_f32 v10, |v10|, |v39|, |v40|
	v_accvgpr_read_b32 v41, a87
	v_max3_f32 v13, |v10|, |v41|, |v41|
	v_mov_b32_e32 v3, v42
	s_nop 1
	v_max_f32_dpp v8, v8, v8 quad_perm:[1,0,3,2] row_mask:0xf bank_mask:0xf
	v_max_f32_dpp v11, v11, v11 quad_perm:[1,0,3,2] row_mask:0xf bank_mask:0xf
	v_max_f32_dpp v12, v12, v12 quad_perm:[1,0,3,2] row_mask:0xf bank_mask:0xf
	v_max_f32_dpp v13, v13, v13 quad_perm:[1,0,3,2] row_mask:0xf bank_mask:0xf
	v_max_f32_dpp v8, v8, v8 quad_perm:[2,3,0,1] row_mask:0xf bank_mask:0xf
	v_max_f32_dpp v11, v11, v11 quad_perm:[2,3,0,1] row_mask:0xf bank_mask:0xf
	v_max_f32_dpp v12, v12, v12 quad_perm:[2,3,0,1] row_mask:0xf bank_mask:0xf
	v_max_f32_dpp v13, v13, v13 quad_perm:[2,3,0,1] row_mask:0xf bank_mask:0xf
	v_max_f32_dpp v8, v8, v8 row_half_mirror row_mask:0xf bank_mask:0xf
	v_max_f32_dpp v11, v11, v11 row_half_mirror row_mask:0xf bank_mask:0xf
	v_max_f32_dpp v12, v12, v12 row_half_mirror row_mask:0xf bank_mask:0xf
	v_max_f32_dpp v13, v13, v13 row_half_mirror row_mask:0xf bank_mask:0xf
	v_max_f32_dpp v8, v8, v8 row_mirror row_mask:0xf bank_mask:0xf
	v_max_f32_dpp v11, v11, v11 row_mirror row_mask:0xf bank_mask:0xf
	v_max_f32_dpp v12, v12, v12 row_mirror row_mask:0xf bank_mask:0xf
	v_max_f32_dpp v13, v13, v13 row_mirror row_mask:0xf bank_mask:0xf
	s_nop 0
	ds_swizzle_b32 v232, v8 offset:swizzle(SWAP,16)
	ds_swizzle_b32 v233, v11 offset:swizzle(SWAP,16)
	ds_swizzle_b32 v234, v12 offset:swizzle(SWAP,16)
	ds_swizzle_b32 v235, v13 offset:swizzle(SWAP,16)
	s_waitcnt lgkmcnt(0)
	v_max_f32_e32 v10, v8, v232
	v_rcp_f32_e32 v8, v10
	v_cmp_lt_f32_e32 vcc, 0, v10
	s_waitcnt lgkmcnt(0)
	v_max_f32_e32 v11, v11, v233
	v_mov_b32_e32 v18, v43
	s_mov_b64 s[6:7], 0x1000
	v_cndmask_b32_e32 v42, 0, v8, vcc
	v_mul_f32_e32 v3, v42, v3
	v_mul_f32_e32 v6, v42, v6
	v_cvt_pknorm_i16_f32 v6, v3, v6
	v_mul_f32_e32 v3, v42, v7
	v_mul_f32_e32 v7, v42, v9
	v_cvt_pknorm_i16_f32 v7, v3, v7
	v_pk_mul_f32 v[224:225], v[14:15], v[42:43] op_sel_hi:[1,0]
	v_pk_mul_f32 v[226:227], v[16:17], v[42:43] op_sel_hi:[1,0]
	v_cvt_pknorm_i16_f32 v8, v224, v225
	v_cvt_pknorm_i16_f32 v9, v226, v227
	v_rcp_f32_e32 v3, v11
	v_cmp_lt_f32_e32 vcc, 0, v11
	v_lshl_add_u64 v[14:15], v[4:5], 0, s[6:7]
	global_store_dwordx4 v[14:15], v[6:9], off sc0 sc1
	v_cndmask_b32_e32 v3, 0, v3, vcc
	v_pk_mul_f32 v[228:229], v[18:19], v[2:3] op_sel:[0,1] op_sel_hi:[1,1]
	v_pk_mul_f32 v[230:231], v[20:21], v[2:3] op_sel:[0,1] op_sel_hi:[1,1]
	v_cvt_pknorm_i16_f32 v6, v228, v229
	v_cvt_pknorm_i16_f32 v7, v230, v231
	v_pk_mul_f32 v[224:225], v[22:23], v[2:3] op_sel:[0,1] op_sel_hi:[1,1]
	v_pk_mul_f32 v[226:227], v[24:25], v[2:3] op_sel:[0,1] op_sel_hi:[1,1]
	v_cvt_pknorm_i16_f32 v8, v224, v225
	s_waitcnt lgkmcnt(0)
	v_max_f32_e32 v12, v12, v234
	v_cvt_pknorm_i16_f32 v9, v226, v227
	v_rcp_f32_e32 v3, v12
	s_mov_b64 s[6:7], 0x1200
	v_cmp_lt_f32_e32 vcc, 0, v12
	v_mov_b32_e32 v26, v44
	v_lshl_add_u64 v[14:15], v[4:5], 0, s[6:7]
	global_store_dwordx4 v[14:15], v[6:9], off sc0 sc1
	s_nop 1
	v_pk_mul_f32 v[6:7], v[10:11], s[4:5] op_sel_hi:[1,0]
	v_cndmask_b32_e32 v3, 0, v3, vcc
	global_store_dwordx2 v0, v[6:7], s[2:3] offset:32
	v_pk_mul_f32 v[228:229], v[26:27], v[2:3] op_sel:[0,1] op_sel_hi:[1,1]
	v_pk_mul_f32 v[230:231], v[28:29], v[2:3] op_sel:[0,1] op_sel_hi:[1,1]
	v_cvt_pknorm_i16_f32 v6, v228, v229
	v_cvt_pknorm_i16_f32 v7, v230, v231
	v_pk_mul_f32 v[224:225], v[30:31], v[2:3] op_sel:[0,1] op_sel_hi:[1,1]
	v_pk_mul_f32 v[226:227], v[32:33], v[2:3] op_sel:[0,1] op_sel_hi:[1,1]
	v_cvt_pknorm_i16_f32 v8, v224, v225
	s_waitcnt lgkmcnt(0)
	v_max_f32_e32 v13, v13, v235
	v_cvt_pknorm_i16_f32 v9, v226, v227
	v_rcp_f32_e32 v3, v13
	v_cmp_lt_f32_e32 vcc, 0, v13
	v_mov_b32_e32 v34, v45
	s_mov_b64 s[6:7], 0x1400
	v_cndmask_b32_e32 v3, 0, v3, vcc
	v_lshl_add_u64 v[10:11], v[4:5], 0, s[6:7]
	global_store_dwordx4 v[10:11], v[6:9], off sc0 sc1
	v_pk_mul_f32 v[228:229], v[34:35], v[2:3] op_sel:[0,1] op_sel_hi:[1,1]
	v_pk_mul_f32 v[230:231], v[36:37], v[2:3] op_sel:[0,1] op_sel_hi:[1,1]
	v_cvt_pknorm_i16_f32 v6, v228, v229
	v_cvt_pknorm_i16_f32 v7, v230, v231
	v_pk_mul_f32 v[224:225], v[38:39], v[2:3] op_sel:[0,1] op_sel_hi:[1,1]
	v_pk_mul_f32 v[226:227], v[40:41], v[2:3] op_sel:[0,1] op_sel_hi:[1,1]
	v_cvt_pknorm_i16_f32 v8, v224, v225
	s_mov_b64 s[6:7], 0x1600
	v_cvt_pknorm_i16_f32 v9, v226, v227
	v_lshl_add_u64 v[10:11], v[4:5], 0, s[6:7]
	global_store_dwordx4 v[10:11], v[6:9], off sc0 sc1
	s_nop 1
	v_pk_mul_f32 v[6:7], v[12:13], s[4:5] op_sel_hi:[1,0]
	v_accvgpr_read_b32 v46, a8
	v_accvgpr_read_b32 v47, a9
	v_accvgpr_read_b32 v48, a10
	v_accvgpr_read_b32 v49, a11
	v_accvgpr_read_b32 v50, a12
	v_accvgpr_read_b32 v51, a13
	v_accvgpr_read_b32 v52, a14
	v_accvgpr_read_b32 v53, a15
	global_store_dwordx2 v0, v[6:7], s[2:3] offset:40
	v_mov_b64_e32 v[42:43], v[46:47]
	v_accvgpr_read_b32 v6, a24
	v_accvgpr_read_b32 v7, a40
	v_max3_f32 v8, |v42|, |v6|, |v7|
	v_accvgpr_read_b32 v9, a56
	v_accvgpr_read_b32 v14, a72
	v_max3_f32 v8, |v8|, |v9|, |v14|
	v_accvgpr_read_b32 v15, a120
	v_accvgpr_read_b32 v16, a136
	v_max3_f32 v8, |v8|, |v15|, |v16|
	v_accvgpr_read_b32 v10, a88
	v_accvgpr_read_b32 v17, a88
	v_max3_f32 v8, |v8|, |v17|, |v10|
	v_accvgpr_read_b32 v19, a25
	v_accvgpr_read_b32 v20, a41
	v_max3_f32 v10, |v43|, |v19|, |v20|
	v_accvgpr_read_b32 v21, a57
	v_accvgpr_read_b32 v22, a73
	v_max3_f32 v10, |v10|, |v21|, |v22|
	v_accvgpr_read_b32 v23, a121
	v_accvgpr_read_b32 v24, a137
	v_max3_f32 v10, |v10|, |v23|, |v24|
	v_mov_b64_e32 v[44:45], v[48:49]
	v_accvgpr_read_b32 v25, a89
	v_max3_f32 v11, |v10|, |v25|, |v25|
	v_accvgpr_read_b32 v27, a26
	v_accvgpr_read_b32 v28, a42
	v_max3_f32 v10, |v44|, |v27|, |v28|
	v_accvgpr_read_b32 v29, a58
	v_accvgpr_read_b32 v30, a74
	v_max3_f32 v10, |v10|, |v29|, |v30|
	v_accvgpr_read_b32 v31, a122
	v_accvgpr_read_b32 v32, a138
	v_max3_f32 v10, |v10|, |v31|, |v32|
	v_accvgpr_read_b32 v33, a90
	v_max3_f32 v12, |v10|, |v33|, |v33|
	v_accvgpr_read_b32 v35, a27
	v_accvgpr_read_b32 v36, a43
	v_max3_f32 v10, |v45|, |v35|, |v36|
	v_accvgpr_read_b32 v37, a59
	v_accvgpr_read_b32 v38, a75
	v_max3_f32 v10, |v10|, |v37|, |v38|
	v_accvgpr_read_b32 v39, a123
	v_accvgpr_read_b32 v40, a139
	v_max3_f32 v10, |v10|, |v39|, |v40|
	v_accvgpr_read_b32 v41, a91
	v_max3_f32 v13, |v10|, |v41|, |v41|
	v_mov_b32_e32 v3, v42
	s_nop 1
	v_max_f32_dpp v8, v8, v8 quad_perm:[1,0,3,2] row_mask:0xf bank_mask:0xf
	v_max_f32_dpp v11, v11, v11 quad_perm:[1,0,3,2] row_mask:0xf bank_mask:0xf
	v_max_f32_dpp v12, v12, v12 quad_perm:[1,0,3,2] row_mask:0xf bank_mask:0xf
	v_max_f32_dpp v13, v13, v13 quad_perm:[1,0,3,2] row_mask:0xf bank_mask:0xf
	v_max_f32_dpp v8, v8, v8 quad_perm:[2,3,0,1] row_mask:0xf bank_mask:0xf
	v_max_f32_dpp v11, v11, v11 quad_perm:[2,3,0,1] row_mask:0xf bank_mask:0xf
	v_max_f32_dpp v12, v12, v12 quad_perm:[2,3,0,1] row_mask:0xf bank_mask:0xf
	v_max_f32_dpp v13, v13, v13 quad_perm:[2,3,0,1] row_mask:0xf bank_mask:0xf
	v_max_f32_dpp v8, v8, v8 row_half_mirror row_mask:0xf bank_mask:0xf
	v_max_f32_dpp v11, v11, v11 row_half_mirror row_mask:0xf bank_mask:0xf
	v_max_f32_dpp v12, v12, v12 row_half_mirror row_mask:0xf bank_mask:0xf
	v_max_f32_dpp v13, v13, v13 row_half_mirror row_mask:0xf bank_mask:0xf
	v_max_f32_dpp v8, v8, v8 row_mirror row_mask:0xf bank_mask:0xf
	v_max_f32_dpp v11, v11, v11 row_mirror row_mask:0xf bank_mask:0xf
	v_max_f32_dpp v12, v12, v12 row_mirror row_mask:0xf bank_mask:0xf
	v_max_f32_dpp v13, v13, v13 row_mirror row_mask:0xf bank_mask:0xf
	s_nop 0
	ds_swizzle_b32 v232, v8 offset:swizzle(SWAP,16)
	ds_swizzle_b32 v233, v11 offset:swizzle(SWAP,16)
	ds_swizzle_b32 v234, v12 offset:swizzle(SWAP,16)
	ds_swizzle_b32 v235, v13 offset:swizzle(SWAP,16)
	s_waitcnt lgkmcnt(0)
	v_max_f32_e32 v10, v8, v232
	v_rcp_f32_e32 v8, v10
	v_cmp_lt_f32_e32 vcc, 0, v10
	s_waitcnt lgkmcnt(0)
	v_max_f32_e32 v11, v11, v233
	v_mov_b32_e32 v18, v43
	s_mov_b64 s[6:7], 0x2000
	v_cndmask_b32_e32 v42, 0, v8, vcc
	v_mul_f32_e32 v3, v42, v3
	v_mul_f32_e32 v6, v42, v6
	v_cvt_pknorm_i16_f32 v6, v3, v6
	v_mul_f32_e32 v3, v42, v7
	v_mul_f32_e32 v7, v42, v9
	v_cvt_pknorm_i16_f32 v7, v3, v7
	v_pk_mul_f32 v[228:229], v[14:15], v[42:43] op_sel_hi:[1,0]
	v_pk_mul_f32 v[230:231], v[16:17], v[42:43] op_sel_hi:[1,0]
	v_cvt_pknorm_i16_f32 v8, v228, v229
	v_cvt_pknorm_i16_f32 v9, v230, v231
	v_rcp_f32_e32 v3, v11
	v_cmp_lt_f32_e32 vcc, 0, v11
	v_lshl_add_u64 v[14:15], v[4:5], 0, s[6:7]
	global_store_dwordx4 v[14:15], v[6:9], off sc0 sc1
	v_cndmask_b32_e32 v3, 0, v3, vcc
	v_pk_mul_f32 v[224:225], v[18:19], v[2:3] op_sel:[0,1] op_sel_hi:[1,1]
	v_pk_mul_f32 v[226:227], v[20:21], v[2:3] op_sel:[0,1] op_sel_hi:[1,1]
	v_cvt_pknorm_i16_f32 v6, v224, v225
	v_cvt_pknorm_i16_f32 v7, v226, v227
	v_pk_mul_f32 v[228:229], v[22:23], v[2:3] op_sel:[0,1] op_sel_hi:[1,1]
	v_pk_mul_f32 v[230:231], v[24:25], v[2:3] op_sel:[0,1] op_sel_hi:[1,1]
	v_cvt_pknorm_i16_f32 v8, v228, v229
	s_waitcnt lgkmcnt(0)
	v_max_f32_e32 v12, v12, v234
	v_cvt_pknorm_i16_f32 v9, v230, v231
	v_rcp_f32_e32 v3, v12
	s_mov_b64 s[6:7], 0x2200
	v_cmp_lt_f32_e32 vcc, 0, v12
	v_mov_b32_e32 v26, v44
	v_lshl_add_u64 v[14:15], v[4:5], 0, s[6:7]
	global_store_dwordx4 v[14:15], v[6:9], off sc0 sc1
	s_nop 1
	v_pk_mul_f32 v[6:7], v[10:11], s[4:5] op_sel_hi:[1,0]
	v_cndmask_b32_e32 v3, 0, v3, vcc
	global_store_dwordx2 v0, v[6:7], s[2:3] offset:64
	v_pk_mul_f32 v[224:225], v[26:27], v[2:3] op_sel:[0,1] op_sel_hi:[1,1]
	v_pk_mul_f32 v[226:227], v[28:29], v[2:3] op_sel:[0,1] op_sel_hi:[1,1]
	v_cvt_pknorm_i16_f32 v6, v224, v225
	v_cvt_pknorm_i16_f32 v7, v226, v227
	v_pk_mul_f32 v[228:229], v[30:31], v[2:3] op_sel:[0,1] op_sel_hi:[1,1]
	v_pk_mul_f32 v[230:231], v[32:33], v[2:3] op_sel:[0,1] op_sel_hi:[1,1]
	v_cvt_pknorm_i16_f32 v8, v228, v229
	s_waitcnt lgkmcnt(0)
	v_max_f32_e32 v13, v13, v235
	v_cvt_pknorm_i16_f32 v9, v230, v231
	v_rcp_f32_e32 v3, v13
	v_cmp_lt_f32_e32 vcc, 0, v13
	v_mov_b32_e32 v34, v45
	s_mov_b64 s[6:7], 0x2400
	v_cndmask_b32_e32 v3, 0, v3, vcc
	v_lshl_add_u64 v[10:11], v[4:5], 0, s[6:7]
	global_store_dwordx4 v[10:11], v[6:9], off sc0 sc1
	v_pk_mul_f32 v[224:225], v[34:35], v[2:3] op_sel:[0,1] op_sel_hi:[1,1]
	v_pk_mul_f32 v[226:227], v[36:37], v[2:3] op_sel:[0,1] op_sel_hi:[1,1]
	v_cvt_pknorm_i16_f32 v6, v224, v225
	v_cvt_pknorm_i16_f32 v7, v226, v227
	v_pk_mul_f32 v[228:229], v[38:39], v[2:3] op_sel:[0,1] op_sel_hi:[1,1]
	v_pk_mul_f32 v[230:231], v[40:41], v[2:3] op_sel:[0,1] op_sel_hi:[1,1]
	v_cvt_pknorm_i16_f32 v8, v228, v229
	s_mov_b64 s[6:7], 0x2600
	v_cvt_pknorm_i16_f32 v9, v230, v231
	v_lshl_add_u64 v[10:11], v[4:5], 0, s[6:7]
	global_store_dwordx4 v[10:11], v[6:9], off sc0 sc1
	s_nop 1
	v_pk_mul_f32 v[6:7], v[12:13], s[4:5] op_sel_hi:[1,0]
	v_mov_b64_e32 v[46:47], v[50:51]
	v_mov_b64_e32 v[48:49], v[52:53]
	global_store_dwordx2 v0, v[6:7], s[2:3] offset:72
	v_mov_b64_e32 v[32:33], v[46:47]
	v_accvgpr_read_b32 v6, a28
	v_accvgpr_read_b32 v7, a44
	v_max3_f32 v8, |v32|, |v6|, |v7|
	v_accvgpr_read_b32 v9, a60
	v_accvgpr_read_b32 v14, a76
	v_max3_f32 v8, |v8|, |v9|, |v14|
	v_accvgpr_read_b32 v15, a124
	v_accvgpr_read_b32 v16, a140
	v_max3_f32 v8, |v8|, |v15|, |v16|
	v_accvgpr_read_b32 v10, a92
	v_accvgpr_read_b32 v17, a92
	v_max3_f32 v8, |v8|, |v17|, |v10|
	v_accvgpr_read_b32 v19, a29
	v_accvgpr_read_b32 v20, a45
	v_max3_f32 v10, |v33|, |v19|, |v20|
	v_accvgpr_read_b32 v21, a61
	v_accvgpr_read_b32 v22, a77
	v_max3_f32 v10, |v10|, |v21|, |v22|
	v_accvgpr_read_b32 v23, a125
	v_accvgpr_read_b32 v24, a141
	v_max3_f32 v10, |v10|, |v23|, |v24|
	v_mov_b64_e32 v[34:35], v[48:49]
	v_accvgpr_read_b32 v25, a93
	v_max3_f32 v11, |v10|, |v25|, |v25|
	v_accvgpr_read_b32 v27, a30
	v_accvgpr_read_b32 v28, a46
	v_max3_f32 v10, |v34|, |v27|, |v28|
	v_accvgpr_read_b32 v29, a62
	v_accvgpr_read_b32 v30, a78
	v_max3_f32 v10, |v10|, |v29|, |v30|
	v_mov_b32_e32 v3, v32
	v_accvgpr_read_b32 v31, a126
	v_accvgpr_read_b32 v32, a142
	v_max3_f32 v10, |v10|, |v31|, |v32|
	v_mov_b32_e32 v18, v33
	v_mov_b32_e32 v26, v34
	v_accvgpr_read_b32 v33, a94
	v_max3_f32 v12, |v10|, |v33|, |v33|
	v_mov_b32_e32 v34, v35
	v_accvgpr_read_b32 v35, a31
	v_accvgpr_read_b32 v36, a47
	v_max3_f32 v10, |v34|, |v35|, |v36|
	v_accvgpr_read_b32 v37, a63
	v_accvgpr_read_b32 v38, a79
	v_max3_f32 v10, |v10|, |v37|, |v38|
	v_accvgpr_read_b32 v39, a127
	v_accvgpr_read_b32 v40, a143
	v_max3_f32 v10, |v10|, |v39|, |v40|
	v_accvgpr_read_b32 v41, a95
	v_max3_f32 v13, |v10|, |v41|, |v41|
	s_mov_b64 s[6:7], 0x3000
	s_nop 1
	v_max_f32_dpp v8, v8, v8 quad_perm:[1,0,3,2] row_mask:0xf bank_mask:0xf
	v_max_f32_dpp v11, v11, v11 quad_perm:[1,0,3,2] row_mask:0xf bank_mask:0xf
	v_max_f32_dpp v12, v12, v12 quad_perm:[1,0,3,2] row_mask:0xf bank_mask:0xf
	v_max_f32_dpp v13, v13, v13 quad_perm:[1,0,3,2] row_mask:0xf bank_mask:0xf
	v_max_f32_dpp v8, v8, v8 quad_perm:[2,3,0,1] row_mask:0xf bank_mask:0xf
	v_max_f32_dpp v11, v11, v11 quad_perm:[2,3,0,1] row_mask:0xf bank_mask:0xf
	v_max_f32_dpp v12, v12, v12 quad_perm:[2,3,0,1] row_mask:0xf bank_mask:0xf
	v_max_f32_dpp v13, v13, v13 quad_perm:[2,3,0,1] row_mask:0xf bank_mask:0xf
	v_max_f32_dpp v8, v8, v8 row_half_mirror row_mask:0xf bank_mask:0xf
	v_max_f32_dpp v11, v11, v11 row_half_mirror row_mask:0xf bank_mask:0xf
	v_max_f32_dpp v12, v12, v12 row_half_mirror row_mask:0xf bank_mask:0xf
	v_max_f32_dpp v13, v13, v13 row_half_mirror row_mask:0xf bank_mask:0xf
	v_max_f32_dpp v8, v8, v8 row_mirror row_mask:0xf bank_mask:0xf
	v_max_f32_dpp v11, v11, v11 row_mirror row_mask:0xf bank_mask:0xf
	v_max_f32_dpp v12, v12, v12 row_mirror row_mask:0xf bank_mask:0xf
	v_max_f32_dpp v13, v13, v13 row_mirror row_mask:0xf bank_mask:0xf
	s_nop 0
	ds_swizzle_b32 v232, v8 offset:swizzle(SWAP,16)
	ds_swizzle_b32 v233, v11 offset:swizzle(SWAP,16)
	ds_swizzle_b32 v234, v12 offset:swizzle(SWAP,16)
	ds_swizzle_b32 v235, v13 offset:swizzle(SWAP,16)
	s_waitcnt lgkmcnt(0)
	v_max_f32_e32 v10, v8, v232
	v_rcp_f32_e32 v8, v10
	v_cmp_lt_f32_e32 vcc, 0, v10
	s_waitcnt lgkmcnt(0)
	v_max_f32_e32 v11, v11, v233
	s_waitcnt lgkmcnt(0)
	v_max_f32_e32 v12, v12, v234
	v_cndmask_b32_e32 v42, 0, v8, vcc
	v_mul_f32_e32 v3, v42, v3
	v_mul_f32_e32 v6, v42, v6
	v_cvt_pknorm_i16_f32 v6, v3, v6
	v_mul_f32_e32 v3, v42, v7
	v_mul_f32_e32 v7, v42, v9
	v_cvt_pknorm_i16_f32 v7, v3, v7
	v_pk_mul_f32 v[224:225], v[14:15], v[42:43] op_sel_hi:[1,0]
	v_pk_mul_f32 v[226:227], v[16:17], v[42:43] op_sel_hi:[1,0]
	v_cvt_pknorm_i16_f32 v8, v224, v225
	v_cvt_pknorm_i16_f32 v9, v226, v227
	v_rcp_f32_e32 v3, v11
	v_cmp_lt_f32_e32 vcc, 0, v11
	v_lshl_add_u64 v[14:15], v[4:5], 0, s[6:7]
	global_store_dwordx4 v[14:15], v[6:9], off sc0 sc1
	s_mov_b64 s[6:7], 0x3200
	v_cndmask_b32_e32 v3, 0, v3, vcc
	v_pk_mul_f32 v[228:229], v[18:19], v[2:3] op_sel:[0,1] op_sel_hi:[1,1]
	v_pk_mul_f32 v[230:231], v[20:21], v[2:3] op_sel:[0,1] op_sel_hi:[1,1]
	v_cvt_pknorm_i16_f32 v6, v228, v229
	v_cvt_pknorm_i16_f32 v7, v230, v231
	v_pk_mul_f32 v[224:225], v[22:23], v[2:3] op_sel:[0,1] op_sel_hi:[1,1]
	v_pk_mul_f32 v[226:227], v[24:25], v[2:3] op_sel:[0,1] op_sel_hi:[1,1]
	v_cvt_pknorm_i16_f32 v8, v224, v225
	v_cvt_pknorm_i16_f32 v9, v226, v227
	v_rcp_f32_e32 v3, v12
	v_cmp_lt_f32_e32 vcc, 0, v12
	v_lshl_add_u64 v[14:15], v[4:5], 0, s[6:7]
	global_store_dwordx4 v[14:15], v[6:9], off sc0 sc1
	s_nop 1
	v_pk_mul_f32 v[6:7], v[10:11], s[4:5] op_sel_hi:[1,0]
	v_cndmask_b32_e32 v3, 0, v3, vcc
	global_store_dwordx2 v0, v[6:7], s[2:3] offset:96
	v_pk_mul_f32 v[228:229], v[26:27], v[2:3] op_sel:[0,1] op_sel_hi:[1,1]
	v_pk_mul_f32 v[230:231], v[28:29], v[2:3] op_sel:[0,1] op_sel_hi:[1,1]
	v_cvt_pknorm_i16_f32 v6, v228, v229
	v_cvt_pknorm_i16_f32 v7, v230, v231
	v_pk_mul_f32 v[224:225], v[30:31], v[2:3] op_sel:[0,1] op_sel_hi:[1,1]
	v_pk_mul_f32 v[226:227], v[32:33], v[2:3] op_sel:[0,1] op_sel_hi:[1,1]
	v_cvt_pknorm_i16_f32 v8, v224, v225
	s_waitcnt lgkmcnt(0)
	v_max_f32_e32 v13, v13, v235
	v_cvt_pknorm_i16_f32 v9, v226, v227
	v_rcp_f32_e32 v3, v13
	v_cmp_lt_f32_e32 vcc, 0, v13
	s_mov_b64 s[6:7], 0x3400
	v_lshl_add_u64 v[10:11], v[4:5], 0, s[6:7]
	v_cndmask_b32_e32 v3, 0, v3, vcc
	global_store_dwordx4 v[10:11], v[6:9], off sc0 sc1
	v_pk_mul_f32 v[228:229], v[34:35], v[2:3] op_sel:[0,1] op_sel_hi:[1,1]
	v_pk_mul_f32 v[230:231], v[36:37], v[2:3] op_sel:[0,1] op_sel_hi:[1,1]
	v_cvt_pknorm_i16_f32 v6, v228, v229
	v_cvt_pknorm_i16_f32 v7, v230, v231
	v_pk_mul_f32 v[224:225], v[38:39], v[2:3] op_sel:[0,1] op_sel_hi:[1,1]
	v_pk_mul_f32 v[226:227], v[40:41], v[2:3] op_sel:[0,1] op_sel_hi:[1,1]
	v_cvt_pknorm_i16_f32 v8, v224, v225
	s_mov_b64 s[6:7], 0x3600
	v_cvt_pknorm_i16_f32 v9, v226, v227
	v_lshl_add_u64 v[10:11], v[4:5], 0, s[6:7]
	global_store_dwordx4 v[10:11], v[6:9], off sc0 sc1
	s_nop 1
	v_pk_mul_f32 v[6:7], v[12:13], s[4:5] op_sel_hi:[1,0]
	global_store_dwordx2 v0, v[6:7], s[2:3] offset:104
	v_accvgpr_read_b32 v3, a240
	v_accvgpr_read_b32 v6, a224
	v_accvgpr_read_b32 v7, a208
	v_max3_f32 v8, |v3|, |v6|, |v7|
	v_accvgpr_read_b32 v9, a192
	v_accvgpr_read_b32 v14, a176
	v_max3_f32 v8, |v8|, |v9|, |v14|
	v_accvgpr_read_b32 v15, a160
	v_accvgpr_read_b32 v16, a144
	v_max3_f32 v8, |v8|, |v15|, |v16|
	v_accvgpr_read_b32 v10, a96
	v_accvgpr_read_b32 v17, a96
	v_max3_f32 v8, |v8|, |v17|, |v10|
	v_accvgpr_read_b32 v18, a241
	v_accvgpr_read_b32 v19, a225
	v_accvgpr_read_b32 v20, a209
	v_max3_f32 v10, |v18|, |v19|, |v20|
	v_accvgpr_read_b32 v21, a193
	v_accvgpr_read_b32 v22, a177
	v_max3_f32 v10, |v10|, |v21|, |v22|
	v_accvgpr_read_b32 v23, a161
	v_accvgpr_read_b32 v24, a145
	v_max3_f32 v10, |v10|, |v23|, |v24|
	v_accvgpr_read_b32 v25, a97
	v_max3_f32 v11, |v10|, |v25|, |v25|
	v_accvgpr_read_b32 v26, a242
	v_accvgpr_read_b32 v27, a226
	v_accvgpr_read_b32 v28, a210
	v_max3_f32 v10, |v26|, |v27|, |v28|
	v_accvgpr_read_b32 v29, a194
	v_accvgpr_read_b32 v30, a178
	v_max3_f32 v10, |v10|, |v29|, |v30|
	v_accvgpr_read_b32 v31, a162
	v_accvgpr_read_b32 v32, a146
	v_max3_f32 v10, |v10|, |v31|, |v32|
	v_accvgpr_read_b32 v33, a98
	v_max3_f32 v12, |v10|, |v33|, |v33|
	v_accvgpr_read_b32 v34, a243
	v_accvgpr_read_b32 v35, a227
	v_accvgpr_read_b32 v36, a211
	v_max3_f32 v10, |v34|, |v35|, |v36|
	v_accvgpr_read_b32 v37, a195
	v_accvgpr_read_b32 v38, a179
	v_max3_f32 v10, |v10|, |v37|, |v38|
	v_accvgpr_read_b32 v39, a163
	v_accvgpr_read_b32 v40, a147
	v_max3_f32 v10, |v10|, |v39|, |v40|
	v_accvgpr_read_b32 v41, a99
	v_max3_f32 v13, |v10|, |v41|, |v41|
	s_mov_b64 s[6:7], 0x4000
	s_nop 1
	v_max_f32_dpp v8, v8, v8 quad_perm:[1,0,3,2] row_mask:0xf bank_mask:0xf
	v_max_f32_dpp v11, v11, v11 quad_perm:[1,0,3,2] row_mask:0xf bank_mask:0xf
	v_max_f32_dpp v12, v12, v12 quad_perm:[1,0,3,2] row_mask:0xf bank_mask:0xf
	v_max_f32_dpp v13, v13, v13 quad_perm:[1,0,3,2] row_mask:0xf bank_mask:0xf
	v_max_f32_dpp v8, v8, v8 quad_perm:[2,3,0,1] row_mask:0xf bank_mask:0xf
	v_max_f32_dpp v11, v11, v11 quad_perm:[2,3,0,1] row_mask:0xf bank_mask:0xf
	v_max_f32_dpp v12, v12, v12 quad_perm:[2,3,0,1] row_mask:0xf bank_mask:0xf
	v_max_f32_dpp v13, v13, v13 quad_perm:[2,3,0,1] row_mask:0xf bank_mask:0xf
	v_max_f32_dpp v8, v8, v8 row_half_mirror row_mask:0xf bank_mask:0xf
	v_max_f32_dpp v11, v11, v11 row_half_mirror row_mask:0xf bank_mask:0xf
	v_max_f32_dpp v12, v12, v12 row_half_mirror row_mask:0xf bank_mask:0xf
	v_max_f32_dpp v13, v13, v13 row_half_mirror row_mask:0xf bank_mask:0xf
	v_max_f32_dpp v8, v8, v8 row_mirror row_mask:0xf bank_mask:0xf
	v_max_f32_dpp v11, v11, v11 row_mirror row_mask:0xf bank_mask:0xf
	v_max_f32_dpp v12, v12, v12 row_mirror row_mask:0xf bank_mask:0xf
	v_max_f32_dpp v13, v13, v13 row_mirror row_mask:0xf bank_mask:0xf
	s_nop 0
	ds_swizzle_b32 v232, v8 offset:swizzle(SWAP,16)
	ds_swizzle_b32 v233, v11 offset:swizzle(SWAP,16)
	ds_swizzle_b32 v234, v12 offset:swizzle(SWAP,16)
	ds_swizzle_b32 v235, v13 offset:swizzle(SWAP,16)
	s_waitcnt lgkmcnt(0)
	v_max_f32_e32 v10, v8, v232
	v_rcp_f32_e32 v8, v10
	v_cmp_lt_f32_e32 vcc, 0, v10
	s_waitcnt lgkmcnt(0)
	v_max_f32_e32 v11, v11, v233
	s_waitcnt lgkmcnt(0)
	v_max_f32_e32 v12, v12, v234
	v_cndmask_b32_e32 v42, 0, v8, vcc
	v_mul_f32_e32 v3, v42, v3
	v_mul_f32_e32 v6, v42, v6
	v_cvt_pknorm_i16_f32 v6, v3, v6
	v_mul_f32_e32 v3, v42, v7
	v_mul_f32_e32 v7, v42, v9
	v_cvt_pknorm_i16_f32 v7, v3, v7
	v_pk_mul_f32 v[228:229], v[14:15], v[42:43] op_sel_hi:[1,0]
	v_pk_mul_f32 v[230:231], v[16:17], v[42:43] op_sel_hi:[1,0]
	v_cvt_pknorm_i16_f32 v8, v228, v229
	v_cvt_pknorm_i16_f32 v9, v230, v231
	v_rcp_f32_e32 v3, v11
	v_cmp_lt_f32_e32 vcc, 0, v11
	v_lshl_add_u64 v[14:15], v[4:5], 0, s[6:7]
	global_store_dwordx4 v[14:15], v[6:9], off sc0 sc1
	s_mov_b64 s[6:7], 0x4200
	v_cndmask_b32_e32 v3, 0, v3, vcc
	v_pk_mul_f32 v[224:225], v[18:19], v[2:3] op_sel:[0,1] op_sel_hi:[1,1]
	v_pk_mul_f32 v[226:227], v[20:21], v[2:3] op_sel:[0,1] op_sel_hi:[1,1]
	v_cvt_pknorm_i16_f32 v6, v224, v225
	v_cvt_pknorm_i16_f32 v7, v226, v227
	v_pk_mul_f32 v[228:229], v[22:23], v[2:3] op_sel:[0,1] op_sel_hi:[1,1]
	v_pk_mul_f32 v[230:231], v[24:25], v[2:3] op_sel:[0,1] op_sel_hi:[1,1]
	v_cvt_pknorm_i16_f32 v8, v228, v229
	v_cvt_pknorm_i16_f32 v9, v230, v231
	v_rcp_f32_e32 v3, v12
	v_cmp_lt_f32_e32 vcc, 0, v12
	v_lshl_add_u64 v[14:15], v[4:5], 0, s[6:7]
	global_store_dwordx4 v[14:15], v[6:9], off sc0 sc1
	s_nop 1
	v_pk_mul_f32 v[6:7], v[10:11], s[4:5] op_sel_hi:[1,0]
	v_cndmask_b32_e32 v3, 0, v3, vcc
	global_store_dwordx2 v0, v[6:7], s[2:3] offset:128
	v_pk_mul_f32 v[224:225], v[26:27], v[2:3] op_sel:[0,1] op_sel_hi:[1,1]
	v_pk_mul_f32 v[226:227], v[28:29], v[2:3] op_sel:[0,1] op_sel_hi:[1,1]
	v_cvt_pknorm_i16_f32 v6, v224, v225
	v_cvt_pknorm_i16_f32 v7, v226, v227
	v_pk_mul_f32 v[228:229], v[30:31], v[2:3] op_sel:[0,1] op_sel_hi:[1,1]
	v_pk_mul_f32 v[230:231], v[32:33], v[2:3] op_sel:[0,1] op_sel_hi:[1,1]
	v_cvt_pknorm_i16_f32 v8, v228, v229
	s_waitcnt lgkmcnt(0)
	v_max_f32_e32 v13, v13, v235
	v_cvt_pknorm_i16_f32 v9, v230, v231
	v_rcp_f32_e32 v3, v13
	v_cmp_lt_f32_e32 vcc, 0, v13
	s_mov_b64 s[6:7], 0x4400
	v_lshl_add_u64 v[10:11], v[4:5], 0, s[6:7]
	v_cndmask_b32_e32 v3, 0, v3, vcc
	global_store_dwordx4 v[10:11], v[6:9], off sc0 sc1
	v_pk_mul_f32 v[224:225], v[34:35], v[2:3] op_sel:[0,1] op_sel_hi:[1,1]
	v_pk_mul_f32 v[226:227], v[36:37], v[2:3] op_sel:[0,1] op_sel_hi:[1,1]
	v_cvt_pknorm_i16_f32 v6, v224, v225
	v_cvt_pknorm_i16_f32 v7, v226, v227
	v_pk_mul_f32 v[228:229], v[38:39], v[2:3] op_sel:[0,1] op_sel_hi:[1,1]
	v_pk_mul_f32 v[230:231], v[40:41], v[2:3] op_sel:[0,1] op_sel_hi:[1,1]
	v_cvt_pknorm_i16_f32 v8, v228, v229
	s_mov_b64 s[6:7], 0x4600
	v_cvt_pknorm_i16_f32 v9, v230, v231
	v_lshl_add_u64 v[10:11], v[4:5], 0, s[6:7]
	global_store_dwordx4 v[10:11], v[6:9], off sc0 sc1
	s_nop 1
	v_pk_mul_f32 v[6:7], v[12:13], s[4:5] op_sel_hi:[1,0]
	global_store_dwordx2 v0, v[6:7], s[2:3] offset:136
	v_accvgpr_read_b32 v3, a244
	v_accvgpr_read_b32 v6, a228
	v_accvgpr_read_b32 v7, a212
	v_max3_f32 v8, |v3|, |v6|, |v7|
	v_accvgpr_read_b32 v9, a196
	v_accvgpr_read_b32 v14, a180
	v_max3_f32 v8, |v8|, |v9|, |v14|
	v_accvgpr_read_b32 v15, a164
	v_accvgpr_read_b32 v16, a148
	v_max3_f32 v8, |v8|, |v15|, |v16|
	v_accvgpr_read_b32 v10, a100
	v_accvgpr_read_b32 v17, a100
	v_max3_f32 v8, |v8|, |v17|, |v10|
	v_accvgpr_read_b32 v18, a245
	v_accvgpr_read_b32 v19, a229
	v_accvgpr_read_b32 v20, a213
	v_max3_f32 v10, |v18|, |v19|, |v20|
	v_accvgpr_read_b32 v21, a197
	v_accvgpr_read_b32 v22, a181
	v_max3_f32 v10, |v10|, |v21|, |v22|
	v_accvgpr_read_b32 v23, a165
	v_accvgpr_read_b32 v24, a149
	v_max3_f32 v10, |v10|, |v23|, |v24|
	v_accvgpr_read_b32 v25, a101
	v_max3_f32 v11, |v10|, |v25|, |v25|
	v_accvgpr_read_b32 v26, a246
	v_accvgpr_read_b32 v27, a230
	v_accvgpr_read_b32 v28, a214
	v_max3_f32 v10, |v26|, |v27|, |v28|
	v_accvgpr_read_b32 v29, a198
	v_accvgpr_read_b32 v30, a182
	v_max3_f32 v10, |v10|, |v29|, |v30|
	v_accvgpr_read_b32 v31, a166
	v_accvgpr_read_b32 v32, a150
	v_max3_f32 v10, |v10|, |v31|, |v32|
	v_accvgpr_read_b32 v33, a102
	v_max3_f32 v12, |v10|, |v33|, |v33|
	v_accvgpr_read_b32 v34, a247
	v_accvgpr_read_b32 v35, a231
	v_accvgpr_read_b32 v36, a215
	v_max3_f32 v10, |v34|, |v35|, |v36|
	v_accvgpr_read_b32 v37, a199
	v_accvgpr_read_b32 v38, a183
	v_max3_f32 v10, |v10|, |v37|, |v38|
	v_accvgpr_read_b32 v39, a167
	v_accvgpr_read_b32 v40, a151
	v_max3_f32 v10, |v10|, |v39|, |v40|
	v_accvgpr_read_b32 v41, a103
	v_max3_f32 v13, |v10|, |v41|, |v41|
	s_mov_b64 s[6:7], 0x5000
	s_nop 1
	v_max_f32_dpp v8, v8, v8 quad_perm:[1,0,3,2] row_mask:0xf bank_mask:0xf
	v_max_f32_dpp v11, v11, v11 quad_perm:[1,0,3,2] row_mask:0xf bank_mask:0xf
	v_max_f32_dpp v12, v12, v12 quad_perm:[1,0,3,2] row_mask:0xf bank_mask:0xf
	v_max_f32_dpp v13, v13, v13 quad_perm:[1,0,3,2] row_mask:0xf bank_mask:0xf
	v_max_f32_dpp v8, v8, v8 quad_perm:[2,3,0,1] row_mask:0xf bank_mask:0xf
	v_max_f32_dpp v11, v11, v11 quad_perm:[2,3,0,1] row_mask:0xf bank_mask:0xf
	v_max_f32_dpp v12, v12, v12 quad_perm:[2,3,0,1] row_mask:0xf bank_mask:0xf
	v_max_f32_dpp v13, v13, v13 quad_perm:[2,3,0,1] row_mask:0xf bank_mask:0xf
	v_max_f32_dpp v8, v8, v8 row_half_mirror row_mask:0xf bank_mask:0xf
	v_max_f32_dpp v11, v11, v11 row_half_mirror row_mask:0xf bank_mask:0xf
	v_max_f32_dpp v12, v12, v12 row_half_mirror row_mask:0xf bank_mask:0xf
	v_max_f32_dpp v13, v13, v13 row_half_mirror row_mask:0xf bank_mask:0xf
	v_max_f32_dpp v8, v8, v8 row_mirror row_mask:0xf bank_mask:0xf
	v_max_f32_dpp v11, v11, v11 row_mirror row_mask:0xf bank_mask:0xf
	v_max_f32_dpp v12, v12, v12 row_mirror row_mask:0xf bank_mask:0xf
	v_max_f32_dpp v13, v13, v13 row_mirror row_mask:0xf bank_mask:0xf
	s_nop 0
	ds_swizzle_b32 v232, v8 offset:swizzle(SWAP,16)
	ds_swizzle_b32 v233, v11 offset:swizzle(SWAP,16)
	ds_swizzle_b32 v234, v12 offset:swizzle(SWAP,16)
	ds_swizzle_b32 v235, v13 offset:swizzle(SWAP,16)
	s_waitcnt lgkmcnt(0)
	v_max_f32_e32 v10, v8, v232
	v_rcp_f32_e32 v8, v10
	v_cmp_lt_f32_e32 vcc, 0, v10
	s_waitcnt lgkmcnt(0)
	v_max_f32_e32 v11, v11, v233
	s_waitcnt lgkmcnt(0)
	v_max_f32_e32 v12, v12, v234
	v_cndmask_b32_e32 v42, 0, v8, vcc
	v_mul_f32_e32 v3, v42, v3
	v_mul_f32_e32 v6, v42, v6
	v_cvt_pknorm_i16_f32 v6, v3, v6
	v_mul_f32_e32 v3, v42, v7
	v_mul_f32_e32 v7, v42, v9
	v_cvt_pknorm_i16_f32 v7, v3, v7
	v_pk_mul_f32 v[224:225], v[14:15], v[42:43] op_sel_hi:[1,0]
	v_pk_mul_f32 v[226:227], v[16:17], v[42:43] op_sel_hi:[1,0]
	v_cvt_pknorm_i16_f32 v8, v224, v225
	v_cvt_pknorm_i16_f32 v9, v226, v227
	v_rcp_f32_e32 v3, v11
	v_cmp_lt_f32_e32 vcc, 0, v11
	v_lshl_add_u64 v[14:15], v[4:5], 0, s[6:7]
	global_store_dwordx4 v[14:15], v[6:9], off sc0 sc1
	s_mov_b64 s[6:7], 0x5200
	v_cndmask_b32_e32 v3, 0, v3, vcc
	v_pk_mul_f32 v[228:229], v[18:19], v[2:3] op_sel:[0,1] op_sel_hi:[1,1]
	v_pk_mul_f32 v[230:231], v[20:21], v[2:3] op_sel:[0,1] op_sel_hi:[1,1]
	v_cvt_pknorm_i16_f32 v6, v228, v229
	v_cvt_pknorm_i16_f32 v7, v230, v231
	v_pk_mul_f32 v[224:225], v[22:23], v[2:3] op_sel:[0,1] op_sel_hi:[1,1]
	v_pk_mul_f32 v[226:227], v[24:25], v[2:3] op_sel:[0,1] op_sel_hi:[1,1]
	v_cvt_pknorm_i16_f32 v8, v224, v225
	v_cvt_pknorm_i16_f32 v9, v226, v227
	v_rcp_f32_e32 v3, v12
	v_cmp_lt_f32_e32 vcc, 0, v12
	v_lshl_add_u64 v[14:15], v[4:5], 0, s[6:7]
	global_store_dwordx4 v[14:15], v[6:9], off sc0 sc1
	s_nop 1
	v_pk_mul_f32 v[6:7], v[10:11], s[4:5] op_sel_hi:[1,0]
	v_cndmask_b32_e32 v3, 0, v3, vcc
	global_store_dwordx2 v0, v[6:7], s[2:3] offset:160
	v_pk_mul_f32 v[228:229], v[26:27], v[2:3] op_sel:[0,1] op_sel_hi:[1,1]
	v_pk_mul_f32 v[230:231], v[28:29], v[2:3] op_sel:[0,1] op_sel_hi:[1,1]
	v_cvt_pknorm_i16_f32 v6, v228, v229
	v_cvt_pknorm_i16_f32 v7, v230, v231
	v_pk_mul_f32 v[224:225], v[30:31], v[2:3] op_sel:[0,1] op_sel_hi:[1,1]
	v_pk_mul_f32 v[226:227], v[32:33], v[2:3] op_sel:[0,1] op_sel_hi:[1,1]
	v_cvt_pknorm_i16_f32 v8, v224, v225
	s_waitcnt lgkmcnt(0)
	v_max_f32_e32 v13, v13, v235
	v_cvt_pknorm_i16_f32 v9, v226, v227
	v_rcp_f32_e32 v3, v13
	v_cmp_lt_f32_e32 vcc, 0, v13
	s_mov_b64 s[6:7], 0x5400
	v_lshl_add_u64 v[10:11], v[4:5], 0, s[6:7]
	v_cndmask_b32_e32 v3, 0, v3, vcc
	global_store_dwordx4 v[10:11], v[6:9], off sc0 sc1
	v_pk_mul_f32 v[228:229], v[34:35], v[2:3] op_sel:[0,1] op_sel_hi:[1,1]
	v_pk_mul_f32 v[230:231], v[36:37], v[2:3] op_sel:[0,1] op_sel_hi:[1,1]
	v_cvt_pknorm_i16_f32 v6, v228, v229
	v_cvt_pknorm_i16_f32 v7, v230, v231
	v_pk_mul_f32 v[224:225], v[38:39], v[2:3] op_sel:[0,1] op_sel_hi:[1,1]
	v_pk_mul_f32 v[226:227], v[40:41], v[2:3] op_sel:[0,1] op_sel_hi:[1,1]
	v_cvt_pknorm_i16_f32 v8, v224, v225
	s_mov_b64 s[6:7], 0x5600
	v_cvt_pknorm_i16_f32 v9, v226, v227
	v_lshl_add_u64 v[10:11], v[4:5], 0, s[6:7]
	global_store_dwordx4 v[10:11], v[6:9], off sc0 sc1
	s_nop 1
	v_pk_mul_f32 v[6:7], v[12:13], s[4:5] op_sel_hi:[1,0]
	global_store_dwordx2 v0, v[6:7], s[2:3] offset:168
	v_accvgpr_read_b32 v3, a248
	v_accvgpr_read_b32 v6, a232
	v_accvgpr_read_b32 v7, a216
	v_max3_f32 v8, |v3|, |v6|, |v7|
	v_accvgpr_read_b32 v9, a200
	v_accvgpr_read_b32 v14, a184
	v_max3_f32 v8, |v8|, |v9|, |v14|
	v_accvgpr_read_b32 v15, a168
	v_accvgpr_read_b32 v16, a152
	v_max3_f32 v8, |v8|, |v15|, |v16|
	v_accvgpr_read_b32 v10, a104
	v_accvgpr_read_b32 v17, a104
	v_max3_f32 v8, |v8|, |v17|, |v10|
	v_accvgpr_read_b32 v18, a249
	v_accvgpr_read_b32 v19, a233
	v_accvgpr_read_b32 v20, a217
	v_max3_f32 v10, |v18|, |v19|, |v20|
	v_accvgpr_read_b32 v21, a201
	v_accvgpr_read_b32 v22, a185
	v_max3_f32 v10, |v10|, |v21|, |v22|
	v_accvgpr_read_b32 v23, a169
	v_accvgpr_read_b32 v24, a153
	v_max3_f32 v10, |v10|, |v23|, |v24|
	v_accvgpr_read_b32 v25, a105
	v_max3_f32 v11, |v10|, |v25|, |v25|
	v_accvgpr_read_b32 v26, a250
	v_accvgpr_read_b32 v27, a234
	v_accvgpr_read_b32 v28, a218
	v_max3_f32 v10, |v26|, |v27|, |v28|
	v_accvgpr_read_b32 v29, a202
	v_accvgpr_read_b32 v30, a186
	v_max3_f32 v10, |v10|, |v29|, |v30|
	v_accvgpr_read_b32 v31, a170
	v_accvgpr_read_b32 v32, a154
	v_max3_f32 v10, |v10|, |v31|, |v32|
	v_accvgpr_read_b32 v33, a106
	v_max3_f32 v12, |v10|, |v33|, |v33|
	v_accvgpr_read_b32 v34, a251
	v_accvgpr_read_b32 v35, a235
	v_accvgpr_read_b32 v36, a219
	v_max3_f32 v10, |v34|, |v35|, |v36|
	v_accvgpr_read_b32 v37, a203
	v_accvgpr_read_b32 v38, a187
	v_max3_f32 v10, |v10|, |v37|, |v38|
	v_accvgpr_read_b32 v39, a171
	v_accvgpr_read_b32 v40, a155
	v_max3_f32 v10, |v10|, |v39|, |v40|
	v_accvgpr_read_b32 v41, a107
	v_max3_f32 v13, |v10|, |v41|, |v41|
	s_mov_b64 s[6:7], 0x6000
	s_nop 1
	v_max_f32_dpp v8, v8, v8 quad_perm:[1,0,3,2] row_mask:0xf bank_mask:0xf
	v_max_f32_dpp v11, v11, v11 quad_perm:[1,0,3,2] row_mask:0xf bank_mask:0xf
	v_max_f32_dpp v12, v12, v12 quad_perm:[1,0,3,2] row_mask:0xf bank_mask:0xf
	v_max_f32_dpp v13, v13, v13 quad_perm:[1,0,3,2] row_mask:0xf bank_mask:0xf
	v_max_f32_dpp v8, v8, v8 quad_perm:[2,3,0,1] row_mask:0xf bank_mask:0xf
	v_max_f32_dpp v11, v11, v11 quad_perm:[2,3,0,1] row_mask:0xf bank_mask:0xf
	v_max_f32_dpp v12, v12, v12 quad_perm:[2,3,0,1] row_mask:0xf bank_mask:0xf
	v_max_f32_dpp v13, v13, v13 quad_perm:[2,3,0,1] row_mask:0xf bank_mask:0xf
	v_max_f32_dpp v8, v8, v8 row_half_mirror row_mask:0xf bank_mask:0xf
	v_max_f32_dpp v11, v11, v11 row_half_mirror row_mask:0xf bank_mask:0xf
	v_max_f32_dpp v12, v12, v12 row_half_mirror row_mask:0xf bank_mask:0xf
	v_max_f32_dpp v13, v13, v13 row_half_mirror row_mask:0xf bank_mask:0xf
	v_max_f32_dpp v8, v8, v8 row_mirror row_mask:0xf bank_mask:0xf
	v_max_f32_dpp v11, v11, v11 row_mirror row_mask:0xf bank_mask:0xf
	v_max_f32_dpp v12, v12, v12 row_mirror row_mask:0xf bank_mask:0xf
	v_max_f32_dpp v13, v13, v13 row_mirror row_mask:0xf bank_mask:0xf
	s_nop 0
	ds_swizzle_b32 v232, v8 offset:swizzle(SWAP,16)
	ds_swizzle_b32 v233, v11 offset:swizzle(SWAP,16)
	ds_swizzle_b32 v234, v12 offset:swizzle(SWAP,16)
	ds_swizzle_b32 v235, v13 offset:swizzle(SWAP,16)
	s_waitcnt lgkmcnt(0)
	v_max_f32_e32 v10, v8, v232
	v_rcp_f32_e32 v8, v10
	v_cmp_lt_f32_e32 vcc, 0, v10
	s_waitcnt lgkmcnt(0)
	v_max_f32_e32 v11, v11, v233
	s_waitcnt lgkmcnt(0)
	v_max_f32_e32 v12, v12, v234
	v_cndmask_b32_e32 v42, 0, v8, vcc
	v_mul_f32_e32 v3, v42, v3
	v_mul_f32_e32 v6, v42, v6
	v_cvt_pknorm_i16_f32 v6, v3, v6
	v_mul_f32_e32 v3, v42, v7
	v_mul_f32_e32 v7, v42, v9
	v_cvt_pknorm_i16_f32 v7, v3, v7
	v_pk_mul_f32 v[228:229], v[14:15], v[42:43] op_sel_hi:[1,0]
	v_pk_mul_f32 v[230:231], v[16:17], v[42:43] op_sel_hi:[1,0]
	v_cvt_pknorm_i16_f32 v8, v228, v229
	v_cvt_pknorm_i16_f32 v9, v230, v231
	v_rcp_f32_e32 v3, v11
	v_cmp_lt_f32_e32 vcc, 0, v11
	v_lshl_add_u64 v[14:15], v[4:5], 0, s[6:7]
	global_store_dwordx4 v[14:15], v[6:9], off sc0 sc1
	s_mov_b64 s[6:7], 0x6200
	v_cndmask_b32_e32 v3, 0, v3, vcc
	v_pk_mul_f32 v[224:225], v[18:19], v[2:3] op_sel:[0,1] op_sel_hi:[1,1]
	v_pk_mul_f32 v[226:227], v[20:21], v[2:3] op_sel:[0,1] op_sel_hi:[1,1]
	v_cvt_pknorm_i16_f32 v6, v224, v225
	v_cvt_pknorm_i16_f32 v7, v226, v227
	v_pk_mul_f32 v[228:229], v[22:23], v[2:3] op_sel:[0,1] op_sel_hi:[1,1]
	v_pk_mul_f32 v[230:231], v[24:25], v[2:3] op_sel:[0,1] op_sel_hi:[1,1]
	v_cvt_pknorm_i16_f32 v8, v228, v229
	v_cvt_pknorm_i16_f32 v9, v230, v231
	v_rcp_f32_e32 v3, v12
	v_cmp_lt_f32_e32 vcc, 0, v12
	v_lshl_add_u64 v[14:15], v[4:5], 0, s[6:7]
	global_store_dwordx4 v[14:15], v[6:9], off sc0 sc1
	s_nop 1
	v_pk_mul_f32 v[6:7], v[10:11], s[4:5] op_sel_hi:[1,0]
	v_cndmask_b32_e32 v3, 0, v3, vcc
	global_store_dwordx2 v0, v[6:7], s[2:3] offset:192
	v_pk_mul_f32 v[224:225], v[26:27], v[2:3] op_sel:[0,1] op_sel_hi:[1,1]
	v_pk_mul_f32 v[226:227], v[28:29], v[2:3] op_sel:[0,1] op_sel_hi:[1,1]
	v_cvt_pknorm_i16_f32 v6, v224, v225
	v_cvt_pknorm_i16_f32 v7, v226, v227
	v_pk_mul_f32 v[228:229], v[30:31], v[2:3] op_sel:[0,1] op_sel_hi:[1,1]
	v_pk_mul_f32 v[230:231], v[32:33], v[2:3] op_sel:[0,1] op_sel_hi:[1,1]
	v_cvt_pknorm_i16_f32 v8, v228, v229
	s_waitcnt lgkmcnt(0)
	v_max_f32_e32 v13, v13, v235
	v_cvt_pknorm_i16_f32 v9, v230, v231
	v_rcp_f32_e32 v3, v13
	v_cmp_lt_f32_e32 vcc, 0, v13
	s_mov_b64 s[6:7], 0x6400
	v_lshl_add_u64 v[10:11], v[4:5], 0, s[6:7]
	v_cndmask_b32_e32 v3, 0, v3, vcc
	global_store_dwordx4 v[10:11], v[6:9], off sc0 sc1
	v_pk_mul_f32 v[224:225], v[34:35], v[2:3] op_sel:[0,1] op_sel_hi:[1,1]
	v_pk_mul_f32 v[226:227], v[36:37], v[2:3] op_sel:[0,1] op_sel_hi:[1,1]
	v_cvt_pknorm_i16_f32 v6, v224, v225
	v_cvt_pknorm_i16_f32 v7, v226, v227
	v_pk_mul_f32 v[228:229], v[38:39], v[2:3] op_sel:[0,1] op_sel_hi:[1,1]
	v_pk_mul_f32 v[230:231], v[40:41], v[2:3] op_sel:[0,1] op_sel_hi:[1,1]
	v_cvt_pknorm_i16_f32 v8, v228, v229
	s_mov_b64 s[6:7], 0x6600
	v_cvt_pknorm_i16_f32 v9, v230, v231
	v_lshl_add_u64 v[10:11], v[4:5], 0, s[6:7]
	global_store_dwordx4 v[10:11], v[6:9], off sc0 sc1
	s_nop 1
	v_pk_mul_f32 v[6:7], v[12:13], s[4:5] op_sel_hi:[1,0]
	global_store_dwordx2 v0, v[6:7], s[2:3] offset:200
	v_accvgpr_read_b32 v3, a252
	v_accvgpr_read_b32 v6, a236
	v_accvgpr_read_b32 v7, a220
	v_max3_f32 v8, |v3|, |v6|, |v7|
	v_accvgpr_read_b32 v9, a204
	v_accvgpr_read_b32 v14, a188
	v_max3_f32 v8, |v8|, |v9|, |v14|
	v_accvgpr_read_b32 v15, a172
	v_accvgpr_read_b32 v16, a156
	v_max3_f32 v8, |v8|, |v15|, |v16|
	v_accvgpr_read_b32 v10, a108
	v_accvgpr_read_b32 v17, a108
	v_max3_f32 v8, |v8|, |v17|, |v10|
	v_accvgpr_read_b32 v18, a253
	v_accvgpr_read_b32 v19, a237
	v_accvgpr_read_b32 v20, a221
	v_max3_f32 v10, |v18|, |v19|, |v20|
	v_accvgpr_read_b32 v21, a205
	v_accvgpr_read_b32 v22, a189
	v_max3_f32 v10, |v10|, |v21|, |v22|
	v_accvgpr_read_b32 v23, a173
	v_accvgpr_read_b32 v24, a157
	v_max3_f32 v10, |v10|, |v23|, |v24|
	v_accvgpr_read_b32 v25, a109
	v_max3_f32 v11, |v10|, |v25|, |v25|
	v_accvgpr_read_b32 v26, a254
	v_accvgpr_read_b32 v27, a238
	v_accvgpr_read_b32 v28, a222
	v_max3_f32 v10, |v26|, |v27|, |v28|
	v_accvgpr_read_b32 v29, a206
	v_accvgpr_read_b32 v30, a190
	v_max3_f32 v10, |v10|, |v29|, |v30|
	v_accvgpr_read_b32 v31, a174
	v_accvgpr_read_b32 v32, a158
	v_max3_f32 v10, |v10|, |v31|, |v32|
	v_accvgpr_read_b32 v33, a110
	v_max3_f32 v12, |v10|, |v33|, |v33|
	v_accvgpr_read_b32 v34, a255
	v_accvgpr_read_b32 v35, a239
	v_accvgpr_read_b32 v36, a223
	v_max3_f32 v10, |v34|, |v35|, |v36|
	v_accvgpr_read_b32 v37, a207
	v_accvgpr_read_b32 v38, a191
	v_max3_f32 v10, |v10|, |v37|, |v38|
	v_accvgpr_read_b32 v39, a175
	v_accvgpr_read_b32 v40, a159
	v_max3_f32 v10, |v10|, |v39|, |v40|
	v_accvgpr_read_b32 v41, a111
	v_max3_f32 v13, |v10|, |v41|, |v41|
	s_mov_b64 s[6:7], 0x7000
	s_nop 1
	v_max_f32_dpp v8, v8, v8 quad_perm:[1,0,3,2] row_mask:0xf bank_mask:0xf
	v_max_f32_dpp v11, v11, v11 quad_perm:[1,0,3,2] row_mask:0xf bank_mask:0xf
	v_max_f32_dpp v12, v12, v12 quad_perm:[1,0,3,2] row_mask:0xf bank_mask:0xf
	v_max_f32_dpp v13, v13, v13 quad_perm:[1,0,3,2] row_mask:0xf bank_mask:0xf
	v_max_f32_dpp v8, v8, v8 quad_perm:[2,3,0,1] row_mask:0xf bank_mask:0xf
	v_max_f32_dpp v11, v11, v11 quad_perm:[2,3,0,1] row_mask:0xf bank_mask:0xf
	v_max_f32_dpp v12, v12, v12 quad_perm:[2,3,0,1] row_mask:0xf bank_mask:0xf
	v_max_f32_dpp v13, v13, v13 quad_perm:[2,3,0,1] row_mask:0xf bank_mask:0xf
	v_max_f32_dpp v8, v8, v8 row_half_mirror row_mask:0xf bank_mask:0xf
	v_max_f32_dpp v11, v11, v11 row_half_mirror row_mask:0xf bank_mask:0xf
	v_max_f32_dpp v12, v12, v12 row_half_mirror row_mask:0xf bank_mask:0xf
	v_max_f32_dpp v13, v13, v13 row_half_mirror row_mask:0xf bank_mask:0xf
	v_max_f32_dpp v8, v8, v8 row_mirror row_mask:0xf bank_mask:0xf
	v_max_f32_dpp v11, v11, v11 row_mirror row_mask:0xf bank_mask:0xf
	v_max_f32_dpp v12, v12, v12 row_mirror row_mask:0xf bank_mask:0xf
	v_max_f32_dpp v13, v13, v13 row_mirror row_mask:0xf bank_mask:0xf
	s_nop 0
	ds_swizzle_b32 v232, v8 offset:swizzle(SWAP,16)
	ds_swizzle_b32 v233, v11 offset:swizzle(SWAP,16)
	ds_swizzle_b32 v234, v12 offset:swizzle(SWAP,16)
	ds_swizzle_b32 v235, v13 offset:swizzle(SWAP,16)
	s_waitcnt lgkmcnt(0)
	v_max_f32_e32 v10, v8, v232
	v_rcp_f32_e32 v8, v10
	v_cmp_lt_f32_e32 vcc, 0, v10
	s_waitcnt lgkmcnt(0)
	v_max_f32_e32 v11, v11, v233
	s_waitcnt lgkmcnt(0)
	v_max_f32_e32 v12, v12, v234
	v_cndmask_b32_e32 v42, 0, v8, vcc
	v_mul_f32_e32 v3, v42, v3
	v_mul_f32_e32 v6, v42, v6
	v_cvt_pknorm_i16_f32 v6, v3, v6
	v_mul_f32_e32 v3, v42, v7
	v_mul_f32_e32 v7, v42, v9
	v_cvt_pknorm_i16_f32 v7, v3, v7
	v_pk_mul_f32 v[224:225], v[14:15], v[42:43] op_sel_hi:[1,0]
	v_pk_mul_f32 v[226:227], v[16:17], v[42:43] op_sel_hi:[1,0]
	v_cvt_pknorm_i16_f32 v8, v224, v225
	v_cvt_pknorm_i16_f32 v9, v226, v227
	v_rcp_f32_e32 v3, v11
	v_cmp_lt_f32_e32 vcc, 0, v11
	v_lshl_add_u64 v[14:15], v[4:5], 0, s[6:7]
	global_store_dwordx4 v[14:15], v[6:9], off sc0 sc1
	s_mov_b64 s[6:7], 0x7200
	v_cndmask_b32_e32 v3, 0, v3, vcc
	v_pk_mul_f32 v[228:229], v[18:19], v[2:3] op_sel:[0,1] op_sel_hi:[1,1]
	v_pk_mul_f32 v[230:231], v[20:21], v[2:3] op_sel:[0,1] op_sel_hi:[1,1]
	v_cvt_pknorm_i16_f32 v6, v228, v229
	v_cvt_pknorm_i16_f32 v7, v230, v231
	v_pk_mul_f32 v[224:225], v[22:23], v[2:3] op_sel:[0,1] op_sel_hi:[1,1]
	v_pk_mul_f32 v[226:227], v[24:25], v[2:3] op_sel:[0,1] op_sel_hi:[1,1]
	v_cvt_pknorm_i16_f32 v8, v224, v225
	v_cvt_pknorm_i16_f32 v9, v226, v227
	v_rcp_f32_e32 v3, v12
	v_cmp_lt_f32_e32 vcc, 0, v12
	v_lshl_add_u64 v[14:15], v[4:5], 0, s[6:7]
	global_store_dwordx4 v[14:15], v[6:9], off sc0 sc1
	s_nop 1
	v_pk_mul_f32 v[6:7], v[10:11], s[4:5] op_sel_hi:[1,0]
	v_cndmask_b32_e32 v3, 0, v3, vcc
	global_store_dwordx2 v0, v[6:7], s[2:3] offset:224
	v_pk_mul_f32 v[228:229], v[26:27], v[2:3] op_sel:[0,1] op_sel_hi:[1,1]
	v_pk_mul_f32 v[230:231], v[28:29], v[2:3] op_sel:[0,1] op_sel_hi:[1,1]
	v_cvt_pknorm_i16_f32 v6, v228, v229
	v_cvt_pknorm_i16_f32 v7, v230, v231
	v_pk_mul_f32 v[224:225], v[30:31], v[2:3] op_sel:[0,1] op_sel_hi:[1,1]
	v_pk_mul_f32 v[226:227], v[32:33], v[2:3] op_sel:[0,1] op_sel_hi:[1,1]
	v_cvt_pknorm_i16_f32 v8, v224, v225
	s_waitcnt lgkmcnt(0)
	v_max_f32_e32 v13, v13, v235
	v_cvt_pknorm_i16_f32 v9, v226, v227
	v_rcp_f32_e32 v3, v13
	v_cmp_lt_f32_e32 vcc, 0, v13
	s_mov_b64 s[6:7], 0x7400
	v_lshl_add_u64 v[10:11], v[4:5], 0, s[6:7]
	v_cndmask_b32_e32 v3, 0, v3, vcc
	global_store_dwordx4 v[10:11], v[6:9], off sc0 sc1
	v_pk_mul_f32 v[228:229], v[34:35], v[2:3] op_sel:[0,1] op_sel_hi:[1,1]
	v_pk_mul_f32 v[230:231], v[36:37], v[2:3] op_sel:[0,1] op_sel_hi:[1,1]
	v_cvt_pknorm_i16_f32 v6, v228, v229
	v_cvt_pknorm_i16_f32 v7, v230, v231
	v_pk_mul_f32 v[224:225], v[38:39], v[2:3] op_sel:[0,1] op_sel_hi:[1,1]
	v_pk_mul_f32 v[226:227], v[40:41], v[2:3] op_sel:[0,1] op_sel_hi:[1,1]
	v_cvt_pknorm_i16_f32 v8, v224, v225
	s_mov_b64 s[6:7], 0x7600
	v_cvt_pknorm_i16_f32 v9, v226, v227
	v_lshl_add_u64 v[4:5], v[4:5], 0, s[6:7]
	global_store_dwordx4 v[4:5], v[6:9], off sc0 sc1
	v_pk_mul_f32 v[4:5], v[12:13], s[4:5] op_sel_hi:[1,0]
	global_store_dwordx2 v0, v[4:5], s[2:3] offset:232
	ds_bpermute_b32 v4, v133, v134
	s_lshl_b64 s[0:1], s[0:1], 2
	s_add_u32 s0, s26, s0
	s_addc_u32 s1, s27, s1
	v_mov_b32_e32 v3, v1
	v_cmp_gt_i32_e32 vcc, 32, v132
	v_lshl_add_u64 v[0:1], s[0:1], 0, v[2:3]
	s_and_saveexec_b64 s[0:1], vcc
	s_cbranch_execz .LBB1_6
	s_waitcnt lgkmcnt(0)
	v_add_f32_e32 v2, v134, v4
	global_store_dword v[0:1], v2, off
